# speedup vs baseline: 1.0045x; 1.0009x over previous
.Lscan_enter_b_st:
	ds_read_b128 v[122:125], v192 offset:0
	ds_read_b64 v[126:127], v192 offset:16
	ds_read_b128 v[128:131], v192 offset:128
	ds_read_b64 v[132:133], v192 offset:144
	s_waitcnt vmcnt(8)
	global_load_dwordx4 v[146:149], v[196:197], off
	global_load_dwordx4 v[150:153], v[196:197], off offset:512
	global_load_dwordx4 v[154:157], v[196:197], off offset:1024
	v_lshl_add_u64 v[196:197], v[196:197], 0, s[42:43]
	s_nop 7
	s_nop 7
	s_waitcnt lgkmcnt(2)
	v_mfma_f32_16x16x128_f8f6f4 v[134:137], v[122:127], v[2:7], 0 cbsz:2 blgp:2
	v_mfma_f32_16x16x128_f8f6f4 v[138:141], v[122:127], v[14:19], 0 cbsz:2 blgp:2
	v_mfma_f32_16x16x128_f8f6f4 v[142:145], v[122:127], v[26:31], v[188:191] cbsz:2 blgp:2
	v_mfma_f32_16x16x128_f8f6f4 v[204:207], v[122:127], v[38:43], 0 cbsz:2 blgp:2
	v_mfma_f32_16x16x128_f8f6f4 v[208:211], v[122:127], v[50:55], 0 cbsz:2 blgp:2
	v_mfma_f32_16x16x128_f8f6f4 v[212:215], v[122:127], v[62:67], v[188:191] cbsz:2 blgp:2
	s_waitcnt lgkmcnt(0)
	v_mfma_f32_16x16x128_f8f6f4 v[134:137], v[128:133], v[8:13], v[134:137] cbsz:2 blgp:2
	v_mfma_f32_16x16x128_f8f6f4 v[204:207], v[128:133], v[44:49], v[204:207] cbsz:2 blgp:2
	v_mfma_f32_16x16x128_f8f6f4 v[138:141], v[128:133], v[20:25], v[138:141] cbsz:2 blgp:2
	v_mfma_f32_16x16x128_f8f6f4 v[208:211], v[128:133], v[56:61], v[208:211] cbsz:2 blgp:2
	v_mfma_f32_16x16x128_f8f6f4 v[142:145], v[128:133], v[32:37], v[142:145] cbsz:2 blgp:2
	v_mfma_f32_16x16x128_f8f6f4 v[212:215], v[128:133], v[68:73], v[212:215] cbsz:2 blgp:2
	v_cndmask_b32_e64 v158, v134, v204, s[4:5]
	v_cndmask_b32_e64 v159, v138, v208, s[4:5]
	v_fma_mix_f32 v158, v158, v1, v82 op_sel_hi:[0,0,1]
	v_fma_mix_f32 v159, v159, v99, v74 op_sel_hi:[0,0,1]
	v_exp_f32_e32 v158, v158
	v_exp_f32_e32 v159, v159
	v_fma_f32 v158, v158, v186, v186
	v_add_f32_e32 v159, 1.0, v159
	v_rcp_f32_e32 v158, v158
	v_rcp_f32_e32 v159, v159
	v_cndmask_b32_e64 v160, v142, v212, s[4:5]
	v_fma_mix_f32 v161, v158, v160, v78 op_sel_hi:[0,0,1]
	v_exp_f32_e32 v161, v161
	s_add_u32 s48, s48, s40
	v_add_f32_e32 v161, 1.0, v161
	v_rcp_f32_e32 v161, v161
	s_addc_u32 s49, s49, s41
	v_fma_f32 v162, v161, -2.0, 1.0
	v_sub_f32_e32 v163, v176, v162
	v_fma_f32 v176, v159, v163, v162
	v_fma_f32 v164, |v176|, s16, v117
	v_fma_f32 v165, |v176|, s17, v118
	v_fma_f32 v166, |v176|, s18, v119
	v_lshrrev_b32_e32 v167, 26, v176
	v_min3_u32 v164, v164, v165, v166
	v_bfi_b32 v168, 31, v164, v167
	s_nop 1
	v_mul_u32_u24_dpp v170, v168, v180 quad_perm:[1,2,3,3] row_mask:0xf bank_mask:0xf bound_ctrl:1
	v_mad_u32_u24 v171, v168, v181, v170
	ds_write_b8_d16_hi v184, v171 offset:544
	s_barrier
	global_store_short_d16_hi v185, v176, s[48:49]
	s_waitcnt lgkmcnt(0)
	s_barrier
	ds_read_b128 v[122:125], v192 offset:544
	ds_read_b64 v[126:127], v192 offset:560
	ds_read_b128 v[128:131], v192 offset:672
	ds_read_b64 v[132:133], v192 offset:688
	s_nop 7
	s_nop 7
	s_waitcnt lgkmcnt(2)
	v_mfma_f32_16x16x128_f8f6f4 v[134:137], v[122:127], v[2:7], 0 cbsz:2 blgp:2
	v_mfma_f32_16x16x128_f8f6f4 v[138:141], v[122:127], v[14:19], 0 cbsz:2 blgp:2
	v_mfma_f32_16x16x128_f8f6f4 v[142:145], v[122:127], v[26:31], v[188:191] cbsz:2 blgp:2
	v_mfma_f32_16x16x128_f8f6f4 v[204:207], v[122:127], v[38:43], 0 cbsz:2 blgp:2
	v_mfma_f32_16x16x128_f8f6f4 v[208:211], v[122:127], v[50:55], 0 cbsz:2 blgp:2
	v_mfma_f32_16x16x128_f8f6f4 v[212:215], v[122:127], v[62:67], v[188:191] cbsz:2 blgp:2
	s_waitcnt lgkmcnt(0)
	v_mfma_f32_16x16x128_f8f6f4 v[134:137], v[128:133], v[8:13], v[134:137] cbsz:2 blgp:2
	v_mfma_f32_16x16x128_f8f6f4 v[204:207], v[128:133], v[44:49], v[204:207] cbsz:2 blgp:2
	v_mfma_f32_16x16x128_f8f6f4 v[138:141], v[128:133], v[20:25], v[138:141] cbsz:2 blgp:2
	v_mfma_f32_16x16x128_f8f6f4 v[208:211], v[128:133], v[56:61], v[208:211] cbsz:2 blgp:2
	v_mfma_f32_16x16x128_f8f6f4 v[142:145], v[128:133], v[32:37], v[142:145] cbsz:2 blgp:2
	v_mfma_f32_16x16x128_f8f6f4 v[212:215], v[128:133], v[68:73], v[212:215] cbsz:2 blgp:2
	v_cndmask_b32_e64 v158, v134, v204, s[4:5]
	v_cndmask_b32_e64 v159, v138, v208, s[4:5]
	v_fma_mix_f32 v158, v158, v1, v82 op_sel:[0,0,1] op_sel_hi:[0,0,1]
	v_fma_mix_f32 v159, v159, v99, v74 op_sel:[0,0,1] op_sel_hi:[0,0,1]
	v_exp_f32_e32 v158, v158
	v_exp_f32_e32 v159, v159
	v_fma_f32 v158, v158, v186, v186
	v_add_f32_e32 v159, 1.0, v159
	v_rcp_f32_e32 v158, v158
	v_rcp_f32_e32 v159, v159
	v_cndmask_b32_e64 v160, v142, v212, s[4:5]
	v_fma_mix_f32 v161, v158, v160, v78 op_sel:[0,0,1] op_sel_hi:[0,0,1]
	v_exp_f32_e32 v161, v161
	s_add_u32 s48, s48, s40
	v_add_f32_e32 v161, 1.0, v161
	v_rcp_f32_e32 v161, v161
	s_addc_u32 s49, s49, s41
	v_fma_f32 v162, v161, -2.0, 1.0
	v_sub_f32_e32 v163, v176, v162
	v_fma_f32 v176, v159, v163, v162
	v_fma_f32 v164, |v176|, s16, v117
	v_fma_f32 v165, |v176|, s17, v118
	v_fma_f32 v166, |v176|, s18, v119
	v_lshrrev_b32_e32 v167, 26, v176
	v_min3_u32 v164, v164, v165, v166
	v_bfi_b32 v168, 31, v164, v167
	s_nop 1
	v_mul_u32_u24_dpp v170, v168, v180 quad_perm:[1,2,3,3] row_mask:0xf bank_mask:0xf bound_ctrl:1
	v_mad_u32_u24 v171, v168, v181, v170
	ds_write_b8_d16_hi v184, v171
	s_barrier
	global_store_short_d16_hi v185, v176, s[48:49]
	s_waitcnt lgkmcnt(0)
	s_barrier
	ds_read_b128 v[122:125], v192 offset:0
	ds_read_b64 v[126:127], v192 offset:16
	ds_read_b128 v[128:131], v192 offset:128
	ds_read_b64 v[132:133], v192 offset:144
	s_nop 7
	s_nop 7
	s_waitcnt lgkmcnt(2)
	v_mfma_f32_16x16x128_f8f6f4 v[134:137], v[122:127], v[2:7], 0 cbsz:2 blgp:2
	v_mfma_f32_16x16x128_f8f6f4 v[138:141], v[122:127], v[14:19], 0 cbsz:2 blgp:2
	v_mfma_f32_16x16x128_f8f6f4 v[142:145], v[122:127], v[26:31], v[188:191] cbsz:2 blgp:2
	v_mfma_f32_16x16x128_f8f6f4 v[204:207], v[122:127], v[38:43], 0 cbsz:2 blgp:2
	v_mfma_f32_16x16x128_f8f6f4 v[208:211], v[122:127], v[50:55], 0 cbsz:2 blgp:2
	v_mfma_f32_16x16x128_f8f6f4 v[212:215], v[122:127], v[62:67], v[188:191] cbsz:2 blgp:2
	s_waitcnt lgkmcnt(0)
	v_mfma_f32_16x16x128_f8f6f4 v[134:137], v[128:133], v[8:13], v[134:137] cbsz:2 blgp:2
	v_mfma_f32_16x16x128_f8f6f4 v[204:207], v[128:133], v[44:49], v[204:207] cbsz:2 blgp:2
	v_mfma_f32_16x16x128_f8f6f4 v[138:141], v[128:133], v[20:25], v[138:141] cbsz:2 blgp:2
	v_mfma_f32_16x16x128_f8f6f4 v[208:211], v[128:133], v[56:61], v[208:211] cbsz:2 blgp:2
	v_mfma_f32_16x16x128_f8f6f4 v[142:145], v[128:133], v[32:37], v[142:145] cbsz:2 blgp:2
	v_mfma_f32_16x16x128_f8f6f4 v[212:215], v[128:133], v[68:73], v[212:215] cbsz:2 blgp:2
	v_cndmask_b32_e64 v158, v134, v204, s[4:5]
	v_cndmask_b32_e64 v159, v138, v208, s[4:5]
	v_fma_mix_f32 v158, v158, v1, v83 op_sel_hi:[0,0,1]
	v_fma_mix_f32 v159, v159, v99, v75 op_sel_hi:[0,0,1]
	v_exp_f32_e32 v158, v158
	v_exp_f32_e32 v159, v159
	v_fma_f32 v158, v158, v186, v186
	v_add_f32_e32 v159, 1.0, v159
	v_rcp_f32_e32 v158, v158
	v_rcp_f32_e32 v159, v159
	v_cndmask_b32_e64 v160, v142, v212, s[4:5]
	v_fma_mix_f32 v161, v158, v160, v79 op_sel_hi:[0,0,1]
	v_exp_f32_e32 v161, v161
	s_add_u32 s48, s48, s40
	v_add_f32_e32 v161, 1.0, v161
	v_rcp_f32_e32 v161, v161
	s_addc_u32 s49, s49, s41
	v_fma_f32 v162, v161, -2.0, 1.0
	v_sub_f32_e32 v163, v176, v162
	v_fma_f32 v176, v159, v163, v162
	v_fma_f32 v164, |v176|, s16, v117
	v_fma_f32 v165, |v176|, s17, v118
	v_fma_f32 v166, |v176|, s18, v119
	v_lshrrev_b32_e32 v167, 26, v176
	v_min3_u32 v164, v164, v165, v166
	v_bfi_b32 v168, 31, v164, v167
	s_nop 1
	v_mul_u32_u24_dpp v170, v168, v180 quad_perm:[1,2,3,3] row_mask:0xf bank_mask:0xf bound_ctrl:1
	v_mad_u32_u24 v171, v168, v181, v170
	ds_write_b8_d16_hi v184, v171 offset:544
	s_barrier
	global_store_short_d16_hi v185, v176, s[48:49]
	s_waitcnt lgkmcnt(0)
	s_barrier
	ds_read_b128 v[122:125], v192 offset:544
	ds_read_b64 v[126:127], v192 offset:560
	ds_read_b128 v[128:131], v192 offset:672
	ds_read_b64 v[132:133], v192 offset:688
	s_nop 7
	s_nop 7
	s_waitcnt lgkmcnt(2)
	v_mfma_f32_16x16x128_f8f6f4 v[134:137], v[122:127], v[2:7], 0 cbsz:2 blgp:2
	v_mfma_f32_16x16x128_f8f6f4 v[138:141], v[122:127], v[14:19], 0 cbsz:2 blgp:2
	v_mfma_f32_16x16x128_f8f6f4 v[142:145], v[122:127], v[26:31], v[188:191] cbsz:2 blgp:2
	v_mfma_f32_16x16x128_f8f6f4 v[204:207], v[122:127], v[38:43], 0 cbsz:2 blgp:2
	v_mfma_f32_16x16x128_f8f6f4 v[208:211], v[122:127], v[50:55], 0 cbsz:2 blgp:2
	v_mfma_f32_16x16x128_f8f6f4 v[212:215], v[122:127], v[62:67], v[188:191] cbsz:2 blgp:2
	s_waitcnt lgkmcnt(0)
	v_mfma_f32_16x16x128_f8f6f4 v[134:137], v[128:133], v[8:13], v[134:137] cbsz:2 blgp:2
	v_mfma_f32_16x16x128_f8f6f4 v[204:207], v[128:133], v[44:49], v[204:207] cbsz:2 blgp:2
	v_mfma_f32_16x16x128_f8f6f4 v[138:141], v[128:133], v[20:25], v[138:141] cbsz:2 blgp:2
	v_mfma_f32_16x16x128_f8f6f4 v[208:211], v[128:133], v[56:61], v[208:211] cbsz:2 blgp:2
	v_mfma_f32_16x16x128_f8f6f4 v[142:145], v[128:133], v[32:37], v[142:145] cbsz:2 blgp:2
	v_mfma_f32_16x16x128_f8f6f4 v[212:215], v[128:133], v[68:73], v[212:215] cbsz:2 blgp:2
	v_cndmask_b32_e64 v158, v134, v204, s[4:5]
	v_cndmask_b32_e64 v159, v138, v208, s[4:5]
	v_fma_mix_f32 v158, v158, v1, v83 op_sel:[0,0,1] op_sel_hi:[0,0,1]
	v_fma_mix_f32 v159, v159, v99, v75 op_sel:[0,0,1] op_sel_hi:[0,0,1]
	v_exp_f32_e32 v158, v158
	v_exp_f32_e32 v159, v159
	v_fma_f32 v158, v158, v186, v186
	v_add_f32_e32 v159, 1.0, v159
	v_rcp_f32_e32 v158, v158
	v_rcp_f32_e32 v159, v159
	v_cndmask_b32_e64 v160, v142, v212, s[4:5]
	v_fma_mix_f32 v161, v158, v160, v79 op_sel:[0,0,1] op_sel_hi:[0,0,1]
	v_exp_f32_e32 v161, v161
	s_add_u32 s48, s48, s40
	v_add_f32_e32 v161, 1.0, v161
	v_rcp_f32_e32 v161, v161
	s_addc_u32 s49, s49, s41
	v_fma_f32 v162, v161, -2.0, 1.0
	v_sub_f32_e32 v163, v176, v162
	v_fma_f32 v176, v159, v163, v162
	v_fma_f32 v164, |v176|, s16, v117
	v_fma_f32 v165, |v176|, s17, v118
	v_fma_f32 v166, |v176|, s18, v119
	v_lshrrev_b32_e32 v167, 26, v176
	v_min3_u32 v164, v164, v165, v166
	v_bfi_b32 v168, 31, v164, v167
	s_nop 1
	v_mul_u32_u24_dpp v170, v168, v180 quad_perm:[1,2,3,3] row_mask:0xf bank_mask:0xf bound_ctrl:1
	v_mad_u32_u24 v171, v168, v181, v170
	ds_write_b8_d16_hi v184, v171
	s_barrier
	global_store_short_d16_hi v185, v176, s[48:49]
	s_waitcnt lgkmcnt(0)
	s_barrier
	ds_read_b128 v[122:125], v192 offset:0
	ds_read_b64 v[126:127], v192 offset:16
	ds_read_b128 v[128:131], v192 offset:128
	ds_read_b64 v[132:133], v192 offset:144
	s_nop 7
	s_nop 7
	s_waitcnt lgkmcnt(2)
	v_mfma_f32_16x16x128_f8f6f4 v[134:137], v[122:127], v[2:7], 0 cbsz:2 blgp:2
	v_mfma_f32_16x16x128_f8f6f4 v[138:141], v[122:127], v[14:19], 0 cbsz:2 blgp:2
	v_mfma_f32_16x16x128_f8f6f4 v[142:145], v[122:127], v[26:31], v[188:191] cbsz:2 blgp:2
	v_mfma_f32_16x16x128_f8f6f4 v[204:207], v[122:127], v[38:43], 0 cbsz:2 blgp:2
	v_mfma_f32_16x16x128_f8f6f4 v[208:211], v[122:127], v[50:55], 0 cbsz:2 blgp:2
	v_mfma_f32_16x16x128_f8f6f4 v[212:215], v[122:127], v[62:67], v[188:191] cbsz:2 blgp:2
	s_waitcnt lgkmcnt(0)
	v_mfma_f32_16x16x128_f8f6f4 v[134:137], v[128:133], v[8:13], v[134:137] cbsz:2 blgp:2
	v_mfma_f32_16x16x128_f8f6f4 v[204:207], v[128:133], v[44:49], v[204:207] cbsz:2 blgp:2
	v_mfma_f32_16x16x128_f8f6f4 v[138:141], v[128:133], v[20:25], v[138:141] cbsz:2 blgp:2
	v_mfma_f32_16x16x128_f8f6f4 v[208:211], v[128:133], v[56:61], v[208:211] cbsz:2 blgp:2
	v_mfma_f32_16x16x128_f8f6f4 v[142:145], v[128:133], v[32:37], v[142:145] cbsz:2 blgp:2
	v_mfma_f32_16x16x128_f8f6f4 v[212:215], v[128:133], v[68:73], v[212:215] cbsz:2 blgp:2
	v_cndmask_b32_e64 v158, v134, v204, s[4:5]
	v_cndmask_b32_e64 v159, v138, v208, s[4:5]
	v_fma_mix_f32 v158, v158, v1, v84 op_sel_hi:[0,0,1]
	v_fma_mix_f32 v159, v159, v99, v76 op_sel_hi:[0,0,1]
	v_exp_f32_e32 v158, v158
	v_exp_f32_e32 v159, v159
	v_fma_f32 v158, v158, v186, v186
	v_add_f32_e32 v159, 1.0, v159
	v_rcp_f32_e32 v158, v158
	v_rcp_f32_e32 v159, v159
	v_cndmask_b32_e64 v160, v142, v212, s[4:5]
	v_fma_mix_f32 v161, v158, v160, v80 op_sel_hi:[0,0,1]
	v_exp_f32_e32 v161, v161
	s_add_u32 s48, s48, s40
	v_add_f32_e32 v161, 1.0, v161
	v_rcp_f32_e32 v161, v161
	s_addc_u32 s49, s49, s41
	v_fma_f32 v162, v161, -2.0, 1.0
	v_sub_f32_e32 v163, v176, v162
	v_fma_f32 v176, v159, v163, v162
	v_fma_f32 v164, |v176|, s16, v117
	v_fma_f32 v165, |v176|, s17, v118
	v_fma_f32 v166, |v176|, s18, v119
	v_lshrrev_b32_e32 v167, 26, v176
	v_min3_u32 v164, v164, v165, v166
	v_bfi_b32 v168, 31, v164, v167
	s_nop 1
	v_mul_u32_u24_dpp v170, v168, v180 quad_perm:[1,2,3,3] row_mask:0xf bank_mask:0xf bound_ctrl:1
	v_mad_u32_u24 v171, v168, v181, v170
	ds_write_b8_d16_hi v184, v171 offset:544
	s_barrier
	global_store_short_d16_hi v185, v176, s[48:49]
	s_waitcnt lgkmcnt(0)
	s_barrier
	ds_read_b128 v[122:125], v192 offset:544
	ds_read_b64 v[126:127], v192 offset:560
	ds_read_b128 v[128:131], v192 offset:672
	ds_read_b64 v[132:133], v192 offset:688
	s_nop 7
	s_nop 7
	s_waitcnt lgkmcnt(2)
	v_mfma_f32_16x16x128_f8f6f4 v[134:137], v[122:127], v[2:7], 0 cbsz:2 blgp:2
	v_mfma_f32_16x16x128_f8f6f4 v[138:141], v[122:127], v[14:19], 0 cbsz:2 blgp:2
	v_mfma_f32_16x16x128_f8f6f4 v[142:145], v[122:127], v[26:31], v[188:191] cbsz:2 blgp:2
	v_mfma_f32_16x16x128_f8f6f4 v[204:207], v[122:127], v[38:43], 0 cbsz:2 blgp:2
	v_mfma_f32_16x16x128_f8f6f4 v[208:211], v[122:127], v[50:55], 0 cbsz:2 blgp:2
	v_mfma_f32_16x16x128_f8f6f4 v[212:215], v[122:127], v[62:67], v[188:191] cbsz:2 blgp:2
	s_waitcnt lgkmcnt(0)
	v_mfma_f32_16x16x128_f8f6f4 v[134:137], v[128:133], v[8:13], v[134:137] cbsz:2 blgp:2
	v_mfma_f32_16x16x128_f8f6f4 v[204:207], v[128:133], v[44:49], v[204:207] cbsz:2 blgp:2
	v_mfma_f32_16x16x128_f8f6f4 v[138:141], v[128:133], v[20:25], v[138:141] cbsz:2 blgp:2
	v_mfma_f32_16x16x128_f8f6f4 v[208:211], v[128:133], v[56:61], v[208:211] cbsz:2 blgp:2
	v_mfma_f32_16x16x128_f8f6f4 v[142:145], v[128:133], v[32:37], v[142:145] cbsz:2 blgp:2
	v_mfma_f32_16x16x128_f8f6f4 v[212:215], v[128:133], v[68:73], v[212:215] cbsz:2 blgp:2
	v_cndmask_b32_e64 v158, v134, v204, s[4:5]
	v_cndmask_b32_e64 v159, v138, v208, s[4:5]
	v_fma_mix_f32 v158, v158, v1, v84 op_sel:[0,0,1] op_sel_hi:[0,0,1]
	v_fma_mix_f32 v159, v159, v99, v76 op_sel:[0,0,1] op_sel_hi:[0,0,1]
	v_exp_f32_e32 v158, v158
	v_exp_f32_e32 v159, v159
	v_fma_f32 v158, v158, v186, v186
	v_add_f32_e32 v159, 1.0, v159
	v_rcp_f32_e32 v158, v158
	v_rcp_f32_e32 v159, v159
	v_cndmask_b32_e64 v160, v142, v212, s[4:5]
	v_fma_mix_f32 v161, v158, v160, v80 op_sel:[0,0,1] op_sel_hi:[0,0,1]
	v_exp_f32_e32 v161, v161
	s_add_u32 s48, s48, s40
	v_add_f32_e32 v161, 1.0, v161
	v_rcp_f32_e32 v161, v161
	s_addc_u32 s49, s49, s41
	v_fma_f32 v162, v161, -2.0, 1.0
	v_sub_f32_e32 v163, v176, v162
	v_fma_f32 v176, v159, v163, v162
	v_fma_f32 v164, |v176|, s16, v117
	v_fma_f32 v165, |v176|, s17, v118
	v_fma_f32 v166, |v176|, s18, v119
	v_lshrrev_b32_e32 v167, 26, v176
	v_min3_u32 v164, v164, v165, v166
	v_bfi_b32 v168, 31, v164, v167
	s_nop 1
	v_mul_u32_u24_dpp v170, v168, v180 quad_perm:[1,2,3,3] row_mask:0xf bank_mask:0xf bound_ctrl:1
	v_mad_u32_u24 v171, v168, v181, v170
	ds_write_b8_d16_hi v184, v171
	s_barrier
	global_store_short_d16_hi v185, v176, s[48:49]
	s_waitcnt lgkmcnt(0)
	s_barrier
	ds_read_b128 v[122:125], v192 offset:0
	ds_read_b64 v[126:127], v192 offset:16
	ds_read_b128 v[128:131], v192 offset:128
	ds_read_b64 v[132:133], v192 offset:144
	s_nop 7
	s_nop 7
	s_waitcnt lgkmcnt(2)
	v_mfma_f32_16x16x128_f8f6f4 v[134:137], v[122:127], v[2:7], 0 cbsz:2 blgp:2
	v_mfma_f32_16x16x128_f8f6f4 v[138:141], v[122:127], v[14:19], 0 cbsz:2 blgp:2
	v_mfma_f32_16x16x128_f8f6f4 v[142:145], v[122:127], v[26:31], v[188:191] cbsz:2 blgp:2
	v_mfma_f32_16x16x128_f8f6f4 v[204:207], v[122:127], v[38:43], 0 cbsz:2 blgp:2
	v_mfma_f32_16x16x128_f8f6f4 v[208:211], v[122:127], v[50:55], 0 cbsz:2 blgp:2
	v_mfma_f32_16x16x128_f8f6f4 v[212:215], v[122:127], v[62:67], v[188:191] cbsz:2 blgp:2
	s_waitcnt lgkmcnt(0)
	v_mfma_f32_16x16x128_f8f6f4 v[134:137], v[128:133], v[8:13], v[134:137] cbsz:2 blgp:2
	v_mfma_f32_16x16x128_f8f6f4 v[204:207], v[128:133], v[44:49], v[204:207] cbsz:2 blgp:2
	v_mfma_f32_16x16x128_f8f6f4 v[138:141], v[128:133], v[20:25], v[138:141] cbsz:2 blgp:2
	v_mfma_f32_16x16x128_f8f6f4 v[208:211], v[128:133], v[56:61], v[208:211] cbsz:2 blgp:2
	v_mfma_f32_16x16x128_f8f6f4 v[142:145], v[128:133], v[32:37], v[142:145] cbsz:2 blgp:2
	v_mfma_f32_16x16x128_f8f6f4 v[212:215], v[128:133], v[68:73], v[212:215] cbsz:2 blgp:2
	v_cndmask_b32_e64 v158, v134, v204, s[4:5]
	v_cndmask_b32_e64 v159, v138, v208, s[4:5]
	v_fma_mix_f32 v158, v158, v1, v85 op_sel_hi:[0,0,1]
	v_fma_mix_f32 v159, v159, v99, v77 op_sel_hi:[0,0,1]
	v_exp_f32_e32 v158, v158
	v_exp_f32_e32 v159, v159
	v_fma_f32 v158, v158, v186, v186
	v_add_f32_e32 v159, 1.0, v159
	v_rcp_f32_e32 v158, v158
	v_rcp_f32_e32 v159, v159
	v_cndmask_b32_e64 v160, v142, v212, s[4:5]
	v_fma_mix_f32 v161, v158, v160, v81 op_sel_hi:[0,0,1]
	v_exp_f32_e32 v161, v161
	s_add_u32 s48, s48, s40
	v_add_f32_e32 v161, 1.0, v161
	v_rcp_f32_e32 v161, v161
	s_addc_u32 s49, s49, s41
	v_fma_f32 v162, v161, -2.0, 1.0
	v_sub_f32_e32 v163, v176, v162
	v_fma_f32 v176, v159, v163, v162
	v_fma_f32 v164, |v176|, s16, v117
	v_fma_f32 v165, |v176|, s17, v118
	v_fma_f32 v166, |v176|, s18, v119
	v_lshrrev_b32_e32 v167, 26, v176
	v_min3_u32 v164, v164, v165, v166
	v_bfi_b32 v168, 31, v164, v167
	s_nop 1
	v_mul_u32_u24_dpp v170, v168, v180 quad_perm:[1,2,3,3] row_mask:0xf bank_mask:0xf bound_ctrl:1
	v_mad_u32_u24 v171, v168, v181, v170
	ds_write_b8_d16_hi v184, v171 offset:544
	s_barrier
	global_store_short_d16_hi v185, v176, s[48:49]
	s_waitcnt lgkmcnt(0)
	s_barrier
	ds_read_b128 v[122:125], v192 offset:544
	ds_read_b64 v[126:127], v192 offset:560
	ds_read_b128 v[128:131], v192 offset:672
	ds_read_b64 v[132:133], v192 offset:688
	s_nop 7
	s_nop 7
	s_waitcnt lgkmcnt(2)
	v_mfma_f32_16x16x128_f8f6f4 v[134:137], v[122:127], v[2:7], 0 cbsz:2 blgp:2
	v_mfma_f32_16x16x128_f8f6f4 v[138:141], v[122:127], v[14:19], 0 cbsz:2 blgp:2
	v_mfma_f32_16x16x128_f8f6f4 v[142:145], v[122:127], v[26:31], v[188:191] cbsz:2 blgp:2
	v_mfma_f32_16x16x128_f8f6f4 v[204:207], v[122:127], v[38:43], 0 cbsz:2 blgp:2
	v_mfma_f32_16x16x128_f8f6f4 v[208:211], v[122:127], v[50:55], 0 cbsz:2 blgp:2
	v_mfma_f32_16x16x128_f8f6f4 v[212:215], v[122:127], v[62:67], v[188:191] cbsz:2 blgp:2
	s_waitcnt lgkmcnt(0)
	v_mfma_f32_16x16x128_f8f6f4 v[134:137], v[128:133], v[8:13], v[134:137] cbsz:2 blgp:2
	v_mfma_f32_16x16x128_f8f6f4 v[204:207], v[128:133], v[44:49], v[204:207] cbsz:2 blgp:2
	v_mfma_f32_16x16x128_f8f6f4 v[138:141], v[128:133], v[20:25], v[138:141] cbsz:2 blgp:2
	v_mfma_f32_16x16x128_f8f6f4 v[208:211], v[128:133], v[56:61], v[208:211] cbsz:2 blgp:2
	v_mfma_f32_16x16x128_f8f6f4 v[142:145], v[128:133], v[32:37], v[142:145] cbsz:2 blgp:2
	v_mfma_f32_16x16x128_f8f6f4 v[212:215], v[128:133], v[68:73], v[212:215] cbsz:2 blgp:2
	v_cndmask_b32_e64 v158, v134, v204, s[4:5]
	v_cndmask_b32_e64 v159, v138, v208, s[4:5]
	v_fma_mix_f32 v158, v158, v1, v85 op_sel:[0,0,1] op_sel_hi:[0,0,1]
	v_fma_mix_f32 v159, v159, v99, v77 op_sel:[0,0,1] op_sel_hi:[0,0,1]
	v_exp_f32_e32 v158, v158
	v_exp_f32_e32 v159, v159
	v_fma_f32 v158, v158, v186, v186
	v_add_f32_e32 v159, 1.0, v159
	v_rcp_f32_e32 v158, v158
	v_rcp_f32_e32 v159, v159
	v_cndmask_b32_e64 v160, v142, v212, s[4:5]
	v_fma_mix_f32 v161, v158, v160, v81 op_sel:[0,0,1] op_sel_hi:[0,0,1]
	v_exp_f32_e32 v161, v161
	s_add_u32 s48, s48, s40
	v_add_f32_e32 v161, 1.0, v161
	v_rcp_f32_e32 v161, v161
	s_addc_u32 s49, s49, s41
	v_fma_f32 v162, v161, -2.0, 1.0
	v_sub_f32_e32 v163, v176, v162
	v_fma_f32 v176, v159, v163, v162
	v_fma_f32 v164, |v176|, s16, v117
	v_fma_f32 v165, |v176|, s17, v118
	v_fma_f32 v166, |v176|, s18, v119
	v_lshrrev_b32_e32 v167, 26, v176
	v_min3_u32 v164, v164, v165, v166
	v_bfi_b32 v168, 31, v164, v167
	s_nop 1
	v_mul_u32_u24_dpp v170, v168, v180 quad_perm:[1,2,3,3] row_mask:0xf bank_mask:0xf bound_ctrl:1
	v_mad_u32_u24 v171, v168, v181, v170
	ds_write_b8_d16_hi v184, v171
	s_barrier
	global_store_short_d16_hi v185, v176, s[48:49]
	s_waitcnt lgkmcnt(0)
	s_barrier
	ds_read_b128 v[122:125], v192 offset:0
	ds_read_b64 v[126:127], v192 offset:16
	ds_read_b128 v[128:131], v192 offset:128
	ds_read_b64 v[132:133], v192 offset:144
	s_waitcnt vmcnt(8)
	global_load_dwordx4 v[82:85], v[196:197], off
	global_load_dwordx4 v[74:77], v[196:197], off offset:512
	global_load_dwordx4 v[78:81], v[196:197], off offset:1024
	v_lshl_add_u64 v[196:197], v[196:197], 0, s[42:43]
	s_nop 7
	s_nop 7
	s_waitcnt lgkmcnt(2)
	v_mfma_f32_16x16x128_f8f6f4 v[134:137], v[122:127], v[2:7], 0 cbsz:2 blgp:2
	v_mfma_f32_16x16x128_f8f6f4 v[138:141], v[122:127], v[14:19], 0 cbsz:2 blgp:2
	v_mfma_f32_16x16x128_f8f6f4 v[142:145], v[122:127], v[26:31], v[188:191] cbsz:2 blgp:2
	v_mfma_f32_16x16x128_f8f6f4 v[204:207], v[122:127], v[38:43], 0 cbsz:2 blgp:2
	v_mfma_f32_16x16x128_f8f6f4 v[208:211], v[122:127], v[50:55], 0 cbsz:2 blgp:2
	v_mfma_f32_16x16x128_f8f6f4 v[212:215], v[122:127], v[62:67], v[188:191] cbsz:2 blgp:2
	s_waitcnt lgkmcnt(0)
	v_mfma_f32_16x16x128_f8f6f4 v[134:137], v[128:133], v[8:13], v[134:137] cbsz:2 blgp:2
	v_mfma_f32_16x16x128_f8f6f4 v[204:207], v[128:133], v[44:49], v[204:207] cbsz:2 blgp:2
	v_mfma_f32_16x16x128_f8f6f4 v[138:141], v[128:133], v[20:25], v[138:141] cbsz:2 blgp:2
	v_mfma_f32_16x16x128_f8f6f4 v[208:211], v[128:133], v[56:61], v[208:211] cbsz:2 blgp:2
	v_mfma_f32_16x16x128_f8f6f4 v[142:145], v[128:133], v[32:37], v[142:145] cbsz:2 blgp:2
	v_mfma_f32_16x16x128_f8f6f4 v[212:215], v[128:133], v[68:73], v[212:215] cbsz:2 blgp:2
	v_cndmask_b32_e64 v158, v134, v204, s[4:5]
	v_cndmask_b32_e64 v159, v138, v208, s[4:5]
	v_fma_mix_f32 v158, v158, v1, v146 op_sel_hi:[0,0,1]
	v_fma_mix_f32 v159, v159, v99, v150 op_sel_hi:[0,0,1]
	v_exp_f32_e32 v158, v158
	v_exp_f32_e32 v159, v159
	v_fma_f32 v158, v158, v186, v186
	v_add_f32_e32 v159, 1.0, v159
	v_rcp_f32_e32 v158, v158
	v_rcp_f32_e32 v159, v159
	v_cndmask_b32_e64 v160, v142, v212, s[4:5]
	v_fma_mix_f32 v161, v158, v160, v154 op_sel_hi:[0,0,1]
	v_exp_f32_e32 v161, v161
	s_add_u32 s48, s48, s40
	v_add_f32_e32 v161, 1.0, v161
	v_rcp_f32_e32 v161, v161
	s_addc_u32 s49, s49, s41
	v_fma_f32 v162, v161, -2.0, 1.0
	v_sub_f32_e32 v163, v176, v162
	v_fma_f32 v176, v159, v163, v162
	v_fma_f32 v164, |v176|, s16, v117
	v_fma_f32 v165, |v176|, s17, v118
	v_fma_f32 v166, |v176|, s18, v119
	v_lshrrev_b32_e32 v167, 26, v176
	v_min3_u32 v164, v164, v165, v166
	v_bfi_b32 v168, 31, v164, v167
	s_nop 1
	v_mul_u32_u24_dpp v170, v168, v180 quad_perm:[1,2,3,3] row_mask:0xf bank_mask:0xf bound_ctrl:1
	v_mad_u32_u24 v171, v168, v181, v170
	ds_write_b8_d16_hi v184, v171 offset:544
	s_barrier
	global_store_short_d16_hi v185, v176, s[48:49]
	s_waitcnt lgkmcnt(0)
	s_barrier
	ds_read_b128 v[122:125], v192 offset:544
	ds_read_b64 v[126:127], v192 offset:560
	ds_read_b128 v[128:131], v192 offset:672
	ds_read_b64 v[132:133], v192 offset:688
	s_nop 7
	s_nop 7
	s_waitcnt lgkmcnt(2)
	v_mfma_f32_16x16x128_f8f6f4 v[134:137], v[122:127], v[2:7], 0 cbsz:2 blgp:2
	v_mfma_f32_16x16x128_f8f6f4 v[138:141], v[122:127], v[14:19], 0 cbsz:2 blgp:2
	v_mfma_f32_16x16x128_f8f6f4 v[142:145], v[122:127], v[26:31], v[188:191] cbsz:2 blgp:2
	v_mfma_f32_16x16x128_f8f6f4 v[204:207], v[122:127], v[38:43], 0 cbsz:2 blgp:2
	v_mfma_f32_16x16x128_f8f6f4 v[208:211], v[122:127], v[50:55], 0 cbsz:2 blgp:2
	v_mfma_f32_16x16x128_f8f6f4 v[212:215], v[122:127], v[62:67], v[188:191] cbsz:2 blgp:2
	s_waitcnt lgkmcnt(0)
	v_mfma_f32_16x16x128_f8f6f4 v[134:137], v[128:133], v[8:13], v[134:137] cbsz:2 blgp:2
	v_mfma_f32_16x16x128_f8f6f4 v[204:207], v[128:133], v[44:49], v[204:207] cbsz:2 blgp:2
	v_mfma_f32_16x16x128_f8f6f4 v[138:141], v[128:133], v[20:25], v[138:141] cbsz:2 blgp:2
	v_mfma_f32_16x16x128_f8f6f4 v[208:211], v[128:133], v[56:61], v[208:211] cbsz:2 blgp:2
	v_mfma_f32_16x16x128_f8f6f4 v[142:145], v[128:133], v[32:37], v[142:145] cbsz:2 blgp:2
	v_mfma_f32_16x16x128_f8f6f4 v[212:215], v[128:133], v[68:73], v[212:215] cbsz:2 blgp:2
	v_cndmask_b32_e64 v158, v134, v204, s[4:5]
	v_cndmask_b32_e64 v159, v138, v208, s[4:5]
	v_fma_mix_f32 v158, v158, v1, v146 op_sel:[0,0,1] op_sel_hi:[0,0,1]
	v_fma_mix_f32 v159, v159, v99, v150 op_sel:[0,0,1] op_sel_hi:[0,0,1]
	v_exp_f32_e32 v158, v158
	v_exp_f32_e32 v159, v159
	v_fma_f32 v158, v158, v186, v186
	v_add_f32_e32 v159, 1.0, v159
	v_rcp_f32_e32 v158, v158
	v_rcp_f32_e32 v159, v159
	v_cndmask_b32_e64 v160, v142, v212, s[4:5]
	v_fma_mix_f32 v161, v158, v160, v154 op_sel:[0,0,1] op_sel_hi:[0,0,1]
	v_exp_f32_e32 v161, v161
	s_add_u32 s48, s48, s40
	v_add_f32_e32 v161, 1.0, v161
	v_rcp_f32_e32 v161, v161
	s_addc_u32 s49, s49, s41
	v_fma_f32 v162, v161, -2.0, 1.0
	v_sub_f32_e32 v163, v176, v162
	v_fma_f32 v176, v159, v163, v162
	v_fma_f32 v164, |v176|, s16, v117
	v_fma_f32 v165, |v176|, s17, v118
	v_fma_f32 v166, |v176|, s18, v119
	v_lshrrev_b32_e32 v167, 26, v176
	v_min3_u32 v164, v164, v165, v166
	v_bfi_b32 v168, 31, v164, v167
	s_nop 1
	v_mul_u32_u24_dpp v170, v168, v180 quad_perm:[1,2,3,3] row_mask:0xf bank_mask:0xf bound_ctrl:1
	v_mad_u32_u24 v171, v168, v181, v170
	ds_write_b8_d16_hi v184, v171
	s_barrier
	global_store_short_d16_hi v185, v176, s[48:49]
	s_waitcnt lgkmcnt(0)
	s_barrier
	ds_read_b128 v[122:125], v192 offset:0
	ds_read_b64 v[126:127], v192 offset:16
	ds_read_b128 v[128:131], v192 offset:128
	ds_read_b64 v[132:133], v192 offset:144
	s_nop 7
	s_nop 7
	s_waitcnt lgkmcnt(2)
	v_mfma_f32_16x16x128_f8f6f4 v[134:137], v[122:127], v[2:7], 0 cbsz:2 blgp:2
	v_mfma_f32_16x16x128_f8f6f4 v[138:141], v[122:127], v[14:19], 0 cbsz:2 blgp:2
	v_mfma_f32_16x16x128_f8f6f4 v[142:145], v[122:127], v[26:31], v[188:191] cbsz:2 blgp:2
	v_mfma_f32_16x16x128_f8f6f4 v[204:207], v[122:127], v[38:43], 0 cbsz:2 blgp:2
	v_mfma_f32_16x16x128_f8f6f4 v[208:211], v[122:127], v[50:55], 0 cbsz:2 blgp:2
	v_mfma_f32_16x16x128_f8f6f4 v[212:215], v[122:127], v[62:67], v[188:191] cbsz:2 blgp:2
	s_waitcnt lgkmcnt(0)
	v_mfma_f32_16x16x128_f8f6f4 v[134:137], v[128:133], v[8:13], v[134:137] cbsz:2 blgp:2
	v_mfma_f32_16x16x128_f8f6f4 v[204:207], v[128:133], v[44:49], v[204:207] cbsz:2 blgp:2
	v_mfma_f32_16x16x128_f8f6f4 v[138:141], v[128:133], v[20:25], v[138:141] cbsz:2 blgp:2
	v_mfma_f32_16x16x128_f8f6f4 v[208:211], v[128:133], v[56:61], v[208:211] cbsz:2 blgp:2
	v_mfma_f32_16x16x128_f8f6f4 v[142:145], v[128:133], v[32:37], v[142:145] cbsz:2 blgp:2
	v_mfma_f32_16x16x128_f8f6f4 v[212:215], v[128:133], v[68:73], v[212:215] cbsz:2 blgp:2
	v_cndmask_b32_e64 v158, v134, v204, s[4:5]
	v_cndmask_b32_e64 v159, v138, v208, s[4:5]
	v_fma_mix_f32 v158, v158, v1, v147 op_sel_hi:[0,0,1]
	v_fma_mix_f32 v159, v159, v99, v151 op_sel_hi:[0,0,1]
	v_exp_f32_e32 v158, v158
	v_exp_f32_e32 v159, v159
	v_fma_f32 v158, v158, v186, v186
	v_add_f32_e32 v159, 1.0, v159
	v_rcp_f32_e32 v158, v158
	v_rcp_f32_e32 v159, v159
	v_cndmask_b32_e64 v160, v142, v212, s[4:5]
	v_fma_mix_f32 v161, v158, v160, v155 op_sel_hi:[0,0,1]
	v_exp_f32_e32 v161, v161
	s_add_u32 s48, s48, s40
	v_add_f32_e32 v161, 1.0, v161
	v_rcp_f32_e32 v161, v161
	s_addc_u32 s49, s49, s41
	v_fma_f32 v162, v161, -2.0, 1.0
	v_sub_f32_e32 v163, v176, v162
	v_fma_f32 v176, v159, v163, v162
	v_fma_f32 v164, |v176|, s16, v117
	v_fma_f32 v165, |v176|, s17, v118
	v_fma_f32 v166, |v176|, s18, v119
	v_lshrrev_b32_e32 v167, 26, v176
	v_min3_u32 v164, v164, v165, v166
	v_bfi_b32 v168, 31, v164, v167
	s_nop 1
	v_mul_u32_u24_dpp v170, v168, v180 quad_perm:[1,2,3,3] row_mask:0xf bank_mask:0xf bound_ctrl:1
	v_mad_u32_u24 v171, v168, v181, v170
	ds_write_b8_d16_hi v184, v171 offset:544
	s_barrier
	global_store_short_d16_hi v185, v176, s[48:49]
	s_waitcnt lgkmcnt(0)
	s_barrier
	ds_read_b128 v[122:125], v192 offset:544
	ds_read_b64 v[126:127], v192 offset:560
	ds_read_b128 v[128:131], v192 offset:672
	ds_read_b64 v[132:133], v192 offset:688
	s_nop 7
	s_nop 7
	s_waitcnt lgkmcnt(2)
	v_mfma_f32_16x16x128_f8f6f4 v[134:137], v[122:127], v[2:7], 0 cbsz:2 blgp:2
	v_mfma_f32_16x16x128_f8f6f4 v[138:141], v[122:127], v[14:19], 0 cbsz:2 blgp:2
	v_mfma_f32_16x16x128_f8f6f4 v[142:145], v[122:127], v[26:31], v[188:191] cbsz:2 blgp:2
	v_mfma_f32_16x16x128_f8f6f4 v[204:207], v[122:127], v[38:43], 0 cbsz:2 blgp:2
	v_mfma_f32_16x16x128_f8f6f4 v[208:211], v[122:127], v[50:55], 0 cbsz:2 blgp:2
	v_mfma_f32_16x16x128_f8f6f4 v[212:215], v[122:127], v[62:67], v[188:191] cbsz:2 blgp:2
	s_waitcnt lgkmcnt(0)
	v_mfma_f32_16x16x128_f8f6f4 v[134:137], v[128:133], v[8:13], v[134:137] cbsz:2 blgp:2
	v_mfma_f32_16x16x128_f8f6f4 v[204:207], v[128:133], v[44:49], v[204:207] cbsz:2 blgp:2
	v_mfma_f32_16x16x128_f8f6f4 v[138:141], v[128:133], v[20:25], v[138:141] cbsz:2 blgp:2
	v_mfma_f32_16x16x128_f8f6f4 v[208:211], v[128:133], v[56:61], v[208:211] cbsz:2 blgp:2
	v_mfma_f32_16x16x128_f8f6f4 v[142:145], v[128:133], v[32:37], v[142:145] cbsz:2 blgp:2
	v_mfma_f32_16x16x128_f8f6f4 v[212:215], v[128:133], v[68:73], v[212:215] cbsz:2 blgp:2
	v_cndmask_b32_e64 v158, v134, v204, s[4:5]
	v_cndmask_b32_e64 v159, v138, v208, s[4:5]
	v_fma_mix_f32 v158, v158, v1, v147 op_sel:[0,0,1] op_sel_hi:[0,0,1]
	v_fma_mix_f32 v159, v159, v99, v151 op_sel:[0,0,1] op_sel_hi:[0,0,1]
	v_exp_f32_e32 v158, v158
	v_exp_f32_e32 v159, v159
	v_fma_f32 v158, v158, v186, v186
	v_add_f32_e32 v159, 1.0, v159
	v_rcp_f32_e32 v158, v158
	v_rcp_f32_e32 v159, v159
	v_cndmask_b32_e64 v160, v142, v212, s[4:5]
	v_fma_mix_f32 v161, v158, v160, v155 op_sel:[0,0,1] op_sel_hi:[0,0,1]
	v_exp_f32_e32 v161, v161
	s_add_u32 s48, s48, s40
	v_add_f32_e32 v161, 1.0, v161
	v_rcp_f32_e32 v161, v161
	s_addc_u32 s49, s49, s41
	v_fma_f32 v162, v161, -2.0, 1.0
	v_sub_f32_e32 v163, v176, v162
	v_fma_f32 v176, v159, v163, v162
	v_fma_f32 v164, |v176|, s16, v117
	v_fma_f32 v165, |v176|, s17, v118
	v_fma_f32 v166, |v176|, s18, v119
	v_lshrrev_b32_e32 v167, 26, v176
	v_min3_u32 v164, v164, v165, v166
	v_bfi_b32 v168, 31, v164, v167
	s_nop 1
	v_mul_u32_u24_dpp v170, v168, v180 quad_perm:[1,2,3,3] row_mask:0xf bank_mask:0xf bound_ctrl:1
	v_mad_u32_u24 v171, v168, v181, v170
	ds_write_b8_d16_hi v184, v171
	s_barrier
	global_store_short_d16_hi v185, v176, s[48:49]
	s_waitcnt lgkmcnt(0)
	s_barrier
	ds_read_b128 v[122:125], v192 offset:0
	ds_read_b64 v[126:127], v192 offset:16
	ds_read_b128 v[128:131], v192 offset:128
	ds_read_b64 v[132:133], v192 offset:144
	s_nop 7
	s_nop 7
	s_waitcnt lgkmcnt(2)
	v_mfma_f32_16x16x128_f8f6f4 v[134:137], v[122:127], v[2:7], 0 cbsz:2 blgp:2
	v_mfma_f32_16x16x128_f8f6f4 v[138:141], v[122:127], v[14:19], 0 cbsz:2 blgp:2
	v_mfma_f32_16x16x128_f8f6f4 v[142:145], v[122:127], v[26:31], v[188:191] cbsz:2 blgp:2
	v_mfma_f32_16x16x128_f8f6f4 v[204:207], v[122:127], v[38:43], 0 cbsz:2 blgp:2
	v_mfma_f32_16x16x128_f8f6f4 v[208:211], v[122:127], v[50:55], 0 cbsz:2 blgp:2
	v_mfma_f32_16x16x128_f8f6f4 v[212:215], v[122:127], v[62:67], v[188:191] cbsz:2 blgp:2
	s_waitcnt lgkmcnt(0)
	v_mfma_f32_16x16x128_f8f6f4 v[134:137], v[128:133], v[8:13], v[134:137] cbsz:2 blgp:2
	v_mfma_f32_16x16x128_f8f6f4 v[204:207], v[128:133], v[44:49], v[204:207] cbsz:2 blgp:2
	v_mfma_f32_16x16x128_f8f6f4 v[138:141], v[128:133], v[20:25], v[138:141] cbsz:2 blgp:2
	v_mfma_f32_16x16x128_f8f6f4 v[208:211], v[128:133], v[56:61], v[208:211] cbsz:2 blgp:2
	v_mfma_f32_16x16x128_f8f6f4 v[142:145], v[128:133], v[32:37], v[142:145] cbsz:2 blgp:2
	v_mfma_f32_16x16x128_f8f6f4 v[212:215], v[128:133], v[68:73], v[212:215] cbsz:2 blgp:2
	v_cndmask_b32_e64 v158, v134, v204, s[4:5]
	v_cndmask_b32_e64 v159, v138, v208, s[4:5]
	v_fma_mix_f32 v158, v158, v1, v148 op_sel_hi:[0,0,1]
	v_fma_mix_f32 v159, v159, v99, v152 op_sel_hi:[0,0,1]
	v_exp_f32_e32 v158, v158
	v_exp_f32_e32 v159, v159
	v_fma_f32 v158, v158, v186, v186
	v_add_f32_e32 v159, 1.0, v159
	v_rcp_f32_e32 v158, v158
	v_rcp_f32_e32 v159, v159
	v_cndmask_b32_e64 v160, v142, v212, s[4:5]
	v_fma_mix_f32 v161, v158, v160, v156 op_sel_hi:[0,0,1]
	v_exp_f32_e32 v161, v161
	s_add_u32 s48, s48, s40
	v_add_f32_e32 v161, 1.0, v161
	v_rcp_f32_e32 v161, v161
	s_addc_u32 s49, s49, s41
	v_fma_f32 v162, v161, -2.0, 1.0
	v_sub_f32_e32 v163, v176, v162
	v_fma_f32 v176, v159, v163, v162
	v_fma_f32 v164, |v176|, s16, v117
	v_fma_f32 v165, |v176|, s17, v118
	v_fma_f32 v166, |v176|, s18, v119
	v_lshrrev_b32_e32 v167, 26, v176
	v_min3_u32 v164, v164, v165, v166
	v_bfi_b32 v168, 31, v164, v167
	s_nop 1
	v_mul_u32_u24_dpp v170, v168, v180 quad_perm:[1,2,3,3] row_mask:0xf bank_mask:0xf bound_ctrl:1
	v_mad_u32_u24 v171, v168, v181, v170
	ds_write_b8_d16_hi v184, v171 offset:544
	s_barrier
	global_store_short_d16_hi v185, v176, s[48:49]
	s_waitcnt lgkmcnt(0)
	s_barrier
	ds_read_b128 v[122:125], v192 offset:544
	ds_read_b64 v[126:127], v192 offset:560
	ds_read_b128 v[128:131], v192 offset:672
	ds_read_b64 v[132:133], v192 offset:688
	s_nop 7
	s_nop 7
	s_waitcnt lgkmcnt(2)
	v_mfma_f32_16x16x128_f8f6f4 v[134:137], v[122:127], v[2:7], 0 cbsz:2 blgp:2
	v_mfma_f32_16x16x128_f8f6f4 v[138:141], v[122:127], v[14:19], 0 cbsz:2 blgp:2
	v_mfma_f32_16x16x128_f8f6f4 v[142:145], v[122:127], v[26:31], v[188:191] cbsz:2 blgp:2
	v_mfma_f32_16x16x128_f8f6f4 v[204:207], v[122:127], v[38:43], 0 cbsz:2 blgp:2
	v_mfma_f32_16x16x128_f8f6f4 v[208:211], v[122:127], v[50:55], 0 cbsz:2 blgp:2
	v_mfma_f32_16x16x128_f8f6f4 v[212:215], v[122:127], v[62:67], v[188:191] cbsz:2 blgp:2
	s_waitcnt lgkmcnt(0)
	v_mfma_f32_16x16x128_f8f6f4 v[134:137], v[128:133], v[8:13], v[134:137] cbsz:2 blgp:2
	v_mfma_f32_16x16x128_f8f6f4 v[204:207], v[128:133], v[44:49], v[204:207] cbsz:2 blgp:2
	v_mfma_f32_16x16x128_f8f6f4 v[138:141], v[128:133], v[20:25], v[138:141] cbsz:2 blgp:2
	v_mfma_f32_16x16x128_f8f6f4 v[208:211], v[128:133], v[56:61], v[208:211] cbsz:2 blgp:2
	v_mfma_f32_16x16x128_f8f6f4 v[142:145], v[128:133], v[32:37], v[142:145] cbsz:2 blgp:2
	v_mfma_f32_16x16x128_f8f6f4 v[212:215], v[128:133], v[68:73], v[212:215] cbsz:2 blgp:2
	v_cndmask_b32_e64 v158, v134, v204, s[4:5]
	v_cndmask_b32_e64 v159, v138, v208, s[4:5]
	v_fma_mix_f32 v158, v158, v1, v148 op_sel:[0,0,1] op_sel_hi:[0,0,1]
	v_fma_mix_f32 v159, v159, v99, v152 op_sel:[0,0,1] op_sel_hi:[0,0,1]
	v_exp_f32_e32 v158, v158
	v_exp_f32_e32 v159, v159
	v_fma_f32 v158, v158, v186, v186
	v_add_f32_e32 v159, 1.0, v159
	v_rcp_f32_e32 v158, v158
	v_rcp_f32_e32 v159, v159
	v_cndmask_b32_e64 v160, v142, v212, s[4:5]
	v_fma_mix_f32 v161, v158, v160, v156 op_sel:[0,0,1] op_sel_hi:[0,0,1]
	v_exp_f32_e32 v161, v161
	s_add_u32 s48, s48, s40
	v_add_f32_e32 v161, 1.0, v161
	v_rcp_f32_e32 v161, v161
	s_addc_u32 s49, s49, s41
	v_fma_f32 v162, v161, -2.0, 1.0
	v_sub_f32_e32 v163, v176, v162
	v_fma_f32 v176, v159, v163, v162
	v_fma_f32 v164, |v176|, s16, v117
	v_fma_f32 v165, |v176|, s17, v118
	v_fma_f32 v166, |v176|, s18, v119
	v_lshrrev_b32_e32 v167, 26, v176
	v_min3_u32 v164, v164, v165, v166
	v_bfi_b32 v168, 31, v164, v167
	s_nop 1
	v_mul_u32_u24_dpp v170, v168, v180 quad_perm:[1,2,3,3] row_mask:0xf bank_mask:0xf bound_ctrl:1
	v_mad_u32_u24 v171, v168, v181, v170
	ds_write_b8_d16_hi v184, v171
	s_barrier
	global_store_short_d16_hi v185, v176, s[48:49]
	s_waitcnt lgkmcnt(0)
	s_barrier
	ds_read_b128 v[122:125], v192 offset:0
	ds_read_b64 v[126:127], v192 offset:16
	ds_read_b128 v[128:131], v192 offset:128
	ds_read_b64 v[132:133], v192 offset:144
	s_nop 7
	s_nop 7
	s_waitcnt lgkmcnt(2)
	v_mfma_f32_16x16x128_f8f6f4 v[134:137], v[122:127], v[2:7], 0 cbsz:2 blgp:2
	v_mfma_f32_16x16x128_f8f6f4 v[138:141], v[122:127], v[14:19], 0 cbsz:2 blgp:2
	v_mfma_f32_16x16x128_f8f6f4 v[142:145], v[122:127], v[26:31], v[188:191] cbsz:2 blgp:2
	v_mfma_f32_16x16x128_f8f6f4 v[204:207], v[122:127], v[38:43], 0 cbsz:2 blgp:2
	v_mfma_f32_16x16x128_f8f6f4 v[208:211], v[122:127], v[50:55], 0 cbsz:2 blgp:2
	v_mfma_f32_16x16x128_f8f6f4 v[212:215], v[122:127], v[62:67], v[188:191] cbsz:2 blgp:2
	s_waitcnt lgkmcnt(0)
	v_mfma_f32_16x16x128_f8f6f4 v[134:137], v[128:133], v[8:13], v[134:137] cbsz:2 blgp:2
	v_mfma_f32_16x16x128_f8f6f4 v[204:207], v[128:133], v[44:49], v[204:207] cbsz:2 blgp:2
	v_mfma_f32_16x16x128_f8f6f4 v[138:141], v[128:133], v[20:25], v[138:141] cbsz:2 blgp:2
	v_mfma_f32_16x16x128_f8f6f4 v[208:211], v[128:133], v[56:61], v[208:211] cbsz:2 blgp:2
	v_mfma_f32_16x16x128_f8f6f4 v[142:145], v[128:133], v[32:37], v[142:145] cbsz:2 blgp:2
	v_mfma_f32_16x16x128_f8f6f4 v[212:215], v[128:133], v[68:73], v[212:215] cbsz:2 blgp:2
	v_cndmask_b32_e64 v158, v134, v204, s[4:5]
	v_cndmask_b32_e64 v159, v138, v208, s[4:5]
	v_fma_mix_f32 v158, v158, v1, v149 op_sel_hi:[0,0,1]
	v_fma_mix_f32 v159, v159, v99, v153 op_sel_hi:[0,0,1]
	v_exp_f32_e32 v158, v158
	v_exp_f32_e32 v159, v159
	v_fma_f32 v158, v158, v186, v186
	v_add_f32_e32 v159, 1.0, v159
	v_rcp_f32_e32 v158, v158
	v_rcp_f32_e32 v159, v159
	v_cndmask_b32_e64 v160, v142, v212, s[4:5]
	v_fma_mix_f32 v161, v158, v160, v157 op_sel_hi:[0,0,1]
	v_exp_f32_e32 v161, v161
	s_add_u32 s48, s48, s40
	v_add_f32_e32 v161, 1.0, v161
	v_rcp_f32_e32 v161, v161
	s_addc_u32 s49, s49, s41
	v_fma_f32 v162, v161, -2.0, 1.0
	v_sub_f32_e32 v163, v176, v162
	v_fma_f32 v176, v159, v163, v162
	v_fma_f32 v164, |v176|, s16, v117
	v_fma_f32 v165, |v176|, s17, v118
	v_fma_f32 v166, |v176|, s18, v119
	v_lshrrev_b32_e32 v167, 26, v176
	v_min3_u32 v164, v164, v165, v166
	v_bfi_b32 v168, 31, v164, v167
	s_nop 1
	v_mul_u32_u24_dpp v170, v168, v180 quad_perm:[1,2,3,3] row_mask:0xf bank_mask:0xf bound_ctrl:1
	v_mad_u32_u24 v171, v168, v181, v170
	ds_write_b8_d16_hi v184, v171 offset:544
	s_barrier
	global_store_short_d16_hi v185, v176, s[48:49]
	s_waitcnt lgkmcnt(0)
	s_barrier
	ds_read_b128 v[122:125], v192 offset:544
	ds_read_b64 v[126:127], v192 offset:560
	ds_read_b128 v[128:131], v192 offset:672
	ds_read_b64 v[132:133], v192 offset:688
	s_add_i32 s44, s44, 16
	s_nop 7
	s_nop 7
	s_waitcnt lgkmcnt(2)
	v_mfma_f32_16x16x128_f8f6f4 v[134:137], v[122:127], v[2:7], 0 cbsz:2 blgp:2
	v_mfma_f32_16x16x128_f8f6f4 v[138:141], v[122:127], v[14:19], 0 cbsz:2 blgp:2
	v_mfma_f32_16x16x128_f8f6f4 v[142:145], v[122:127], v[26:31], v[188:191] cbsz:2 blgp:2
	v_mfma_f32_16x16x128_f8f6f4 v[204:207], v[122:127], v[38:43], 0 cbsz:2 blgp:2
	v_mfma_f32_16x16x128_f8f6f4 v[208:211], v[122:127], v[50:55], 0 cbsz:2 blgp:2
	v_mfma_f32_16x16x128_f8f6f4 v[212:215], v[122:127], v[62:67], v[188:191] cbsz:2 blgp:2
	s_waitcnt lgkmcnt(0)
	v_mfma_f32_16x16x128_f8f6f4 v[134:137], v[128:133], v[8:13], v[134:137] cbsz:2 blgp:2
	v_mfma_f32_16x16x128_f8f6f4 v[204:207], v[128:133], v[44:49], v[204:207] cbsz:2 blgp:2
	v_mfma_f32_16x16x128_f8f6f4 v[138:141], v[128:133], v[20:25], v[138:141] cbsz:2 blgp:2
	v_mfma_f32_16x16x128_f8f6f4 v[208:211], v[128:133], v[56:61], v[208:211] cbsz:2 blgp:2
	v_mfma_f32_16x16x128_f8f6f4 v[142:145], v[128:133], v[32:37], v[142:145] cbsz:2 blgp:2
	v_mfma_f32_16x16x128_f8f6f4 v[212:215], v[128:133], v[68:73], v[212:215] cbsz:2 blgp:2
	v_cndmask_b32_e64 v158, v134, v204, s[4:5]
	v_cndmask_b32_e64 v159, v138, v208, s[4:5]
	v_fma_mix_f32 v158, v158, v1, v149 op_sel:[0,0,1] op_sel_hi:[0,0,1]
	v_fma_mix_f32 v159, v159, v99, v153 op_sel:[0,0,1] op_sel_hi:[0,0,1]
	v_exp_f32_e32 v158, v158
	v_exp_f32_e32 v159, v159
	v_fma_f32 v158, v158, v186, v186
	v_add_f32_e32 v159, 1.0, v159
	v_rcp_f32_e32 v158, v158
	v_rcp_f32_e32 v159, v159
	v_cndmask_b32_e64 v160, v142, v212, s[4:5]
	v_fma_mix_f32 v161, v158, v160, v157 op_sel:[0,0,1] op_sel_hi:[0,0,1]
	v_exp_f32_e32 v161, v161
	s_add_u32 s48, s48, s40
	v_add_f32_e32 v161, 1.0, v161
	v_rcp_f32_e32 v161, v161
	s_addc_u32 s49, s49, s41
	v_fma_f32 v162, v161, -2.0, 1.0
	v_sub_f32_e32 v163, v176, v162
	v_fma_f32 v176, v159, v163, v162
	v_fma_f32 v164, |v176|, s16, v117
	v_fma_f32 v165, |v176|, s17, v118
	v_fma_f32 v166, |v176|, s18, v119
	v_lshrrev_b32_e32 v167, 26, v176
	v_min3_u32 v164, v164, v165, v166
	v_bfi_b32 v168, 31, v164, v167
	s_nop 1
	v_mul_u32_u24_dpp v170, v168, v180 quad_perm:[1,2,3,3] row_mask:0xf bank_mask:0xf bound_ctrl:1
	v_mad_u32_u24 v171, v168, v181, v170
	ds_write_b8_d16_hi v184, v171
	s_barrier
	global_store_short_d16_hi v185, v176, s[48:49]
	s_cmp_lt_i32 s44, s45
	s_cbranch_scc1 .Lscan_loop_b_st
	s_waitcnt lgkmcnt(0)
	s_barrier

.Lscan_enter_b_f2:
	ds_read_b128 v[122:125], v192 offset:0
	ds_read_b64 v[126:127], v192 offset:16
	ds_read_b128 v[128:131], v192 offset:128
	ds_read_b64 v[132:133], v192 offset:144
	s_waitcnt vmcnt(8)
	global_load_dwordx4 v[146:149], v[196:197], off
	global_load_dwordx4 v[150:153], v[196:197], off offset:512
	global_load_dwordx4 v[154:157], v[196:197], off offset:1024
	v_lshl_add_u64 v[196:197], v[196:197], 0, s[42:43]
	s_nop 7
	s_nop 7
	s_waitcnt lgkmcnt(2)
	v_mfma_f32_16x16x128_f8f6f4 v[134:137], v[122:127], v[2:7], 0 cbsz:2 blgp:2
	v_mfma_f32_16x16x128_f8f6f4 v[138:141], v[122:127], v[14:19], 0 cbsz:2 blgp:2
	v_mfma_f32_16x16x128_f8f6f4 v[142:145], v[122:127], v[26:31], v[188:191] cbsz:2 blgp:2
	v_mfma_f32_16x16x128_f8f6f4 v[204:207], v[122:127], v[38:43], 0 cbsz:2 blgp:2
	v_mfma_f32_16x16x128_f8f6f4 v[208:211], v[122:127], v[50:55], 0 cbsz:2 blgp:2
	v_mfma_f32_16x16x128_f8f6f4 v[212:215], v[122:127], v[62:67], v[188:191] cbsz:2 blgp:2
	s_waitcnt lgkmcnt(0)
	v_mfma_f32_16x16x128_f8f6f4 v[134:137], v[128:133], v[8:13], v[134:137] cbsz:2 blgp:2
	v_mfma_f32_16x16x128_f8f6f4 v[204:207], v[128:133], v[44:49], v[204:207] cbsz:2 blgp:2
	v_mfma_f32_16x16x128_f8f6f4 v[138:141], v[128:133], v[20:25], v[138:141] cbsz:2 blgp:2
	v_mfma_f32_16x16x128_f8f6f4 v[208:211], v[128:133], v[56:61], v[208:211] cbsz:2 blgp:2
	v_mfma_f32_16x16x128_f8f6f4 v[142:145], v[128:133], v[32:37], v[142:145] cbsz:2 blgp:2
	v_mfma_f32_16x16x128_f8f6f4 v[212:215], v[128:133], v[68:73], v[212:215] cbsz:2 blgp:2
	v_cndmask_b32_e64 v158, v134, v204, s[0:1]
	v_cndmask_b32_e64 v159, v138, v208, s[0:1]
	v_fma_mix_f32 v158, v158, v100, v82 op_sel_hi:[0,0,1]
	v_fma_mix_f32 v159, v159, v101, v74 op_sel_hi:[0,0,1]
	v_exp_f32_e32 v158, v158
	v_exp_f32_e32 v159, v159
	v_fma_f32 v158, v158, v186, v186
	v_add_f32_e32 v159, 1.0, v159
	v_rcp_f32_e32 v158, v158
	v_rcp_f32_e32 v159, v159
	v_cndmask_b32_e64 v160, v142, v212, s[0:1]
	v_fma_mix_f32 v161, v158, v160, v78 op_sel_hi:[0,0,1]
	v_exp_f32_e32 v161, v161
	s_add_u32 s48, s48, s40
	v_add_f32_e32 v161, 1.0, v161
	v_rcp_f32_e32 v161, v161
	s_addc_u32 s49, s49, s41
	v_fma_f32 v162, v161, -2.0, 1.0
	v_sub_f32_e32 v163, v176, v162
	v_fma_f32 v176, v159, v163, v162
	v_fma_f32 v164, |v176|, s17, v113
	v_fma_f32 v165, |v176|, s18, v114
	v_fma_f32 v166, |v176|, s19, v115
	v_lshrrev_b32_e32 v167, 26, v176
	v_min3_u32 v164, v164, v165, v166
	v_bfi_b32 v168, 31, v164, v167
	s_nop 1
	v_mul_u32_u24_dpp v170, v168, v180 quad_perm:[1,2,3,3] row_mask:0xf bank_mask:0xf bound_ctrl:1
	v_mad_u32_u24 v171, v168, v181, v170
	ds_write_b8_d16_hi v184, v171 offset:544
	s_barrier
	global_store_short_d16_hi v185, v176, s[48:49]
	s_waitcnt lgkmcnt(0)
	s_barrier
	ds_read_b128 v[122:125], v192 offset:544
	ds_read_b64 v[126:127], v192 offset:560
	ds_read_b128 v[128:131], v192 offset:672
	ds_read_b64 v[132:133], v192 offset:688
	s_nop 7
	s_nop 7
	s_waitcnt lgkmcnt(2)
	v_mfma_f32_16x16x128_f8f6f4 v[134:137], v[122:127], v[2:7], 0 cbsz:2 blgp:2
	v_mfma_f32_16x16x128_f8f6f4 v[138:141], v[122:127], v[14:19], 0 cbsz:2 blgp:2
	v_mfma_f32_16x16x128_f8f6f4 v[142:145], v[122:127], v[26:31], v[188:191] cbsz:2 blgp:2
	v_mfma_f32_16x16x128_f8f6f4 v[204:207], v[122:127], v[38:43], 0 cbsz:2 blgp:2
	v_mfma_f32_16x16x128_f8f6f4 v[208:211], v[122:127], v[50:55], 0 cbsz:2 blgp:2
	v_mfma_f32_16x16x128_f8f6f4 v[212:215], v[122:127], v[62:67], v[188:191] cbsz:2 blgp:2
	s_waitcnt lgkmcnt(0)
	v_mfma_f32_16x16x128_f8f6f4 v[134:137], v[128:133], v[8:13], v[134:137] cbsz:2 blgp:2
	v_mfma_f32_16x16x128_f8f6f4 v[204:207], v[128:133], v[44:49], v[204:207] cbsz:2 blgp:2
	v_mfma_f32_16x16x128_f8f6f4 v[138:141], v[128:133], v[20:25], v[138:141] cbsz:2 blgp:2
	v_mfma_f32_16x16x128_f8f6f4 v[208:211], v[128:133], v[56:61], v[208:211] cbsz:2 blgp:2
	v_mfma_f32_16x16x128_f8f6f4 v[142:145], v[128:133], v[32:37], v[142:145] cbsz:2 blgp:2
	v_mfma_f32_16x16x128_f8f6f4 v[212:215], v[128:133], v[68:73], v[212:215] cbsz:2 blgp:2
	v_cndmask_b32_e64 v158, v134, v204, s[0:1]
	v_cndmask_b32_e64 v159, v138, v208, s[0:1]
	v_fma_mix_f32 v158, v158, v100, v82 op_sel:[0,0,1] op_sel_hi:[0,0,1]
	v_fma_mix_f32 v159, v159, v101, v74 op_sel:[0,0,1] op_sel_hi:[0,0,1]
	v_exp_f32_e32 v158, v158
	v_exp_f32_e32 v159, v159
	v_fma_f32 v158, v158, v186, v186
	v_add_f32_e32 v159, 1.0, v159
	v_rcp_f32_e32 v158, v158
	v_rcp_f32_e32 v159, v159
	v_cndmask_b32_e64 v160, v142, v212, s[0:1]
	v_fma_mix_f32 v161, v158, v160, v78 op_sel:[0,0,1] op_sel_hi:[0,0,1]
	v_exp_f32_e32 v161, v161
	s_add_u32 s48, s48, s40
	v_add_f32_e32 v161, 1.0, v161
	v_rcp_f32_e32 v161, v161
	s_addc_u32 s49, s49, s41
	v_fma_f32 v162, v161, -2.0, 1.0
	v_sub_f32_e32 v163, v176, v162
	v_fma_f32 v176, v159, v163, v162
	v_fma_f32 v164, |v176|, s17, v113
	v_fma_f32 v165, |v176|, s18, v114
	v_fma_f32 v166, |v176|, s19, v115
	v_lshrrev_b32_e32 v167, 26, v176
	v_min3_u32 v164, v164, v165, v166
	v_bfi_b32 v168, 31, v164, v167
	s_nop 1
	v_mul_u32_u24_dpp v170, v168, v180 quad_perm:[1,2,3,3] row_mask:0xf bank_mask:0xf bound_ctrl:1
	v_mad_u32_u24 v171, v168, v181, v170
	ds_write_b8_d16_hi v184, v171
	s_barrier
	global_store_short_d16_hi v185, v176, s[48:49]
	s_waitcnt lgkmcnt(0)
	s_barrier
	ds_read_b128 v[122:125], v192 offset:0
	ds_read_b64 v[126:127], v192 offset:16
	ds_read_b128 v[128:131], v192 offset:128
	ds_read_b64 v[132:133], v192 offset:144
	s_nop 7
	s_nop 7
	s_waitcnt lgkmcnt(2)
	v_mfma_f32_16x16x128_f8f6f4 v[134:137], v[122:127], v[2:7], 0 cbsz:2 blgp:2
	v_mfma_f32_16x16x128_f8f6f4 v[138:141], v[122:127], v[14:19], 0 cbsz:2 blgp:2
	v_mfma_f32_16x16x128_f8f6f4 v[142:145], v[122:127], v[26:31], v[188:191] cbsz:2 blgp:2
	v_mfma_f32_16x16x128_f8f6f4 v[204:207], v[122:127], v[38:43], 0 cbsz:2 blgp:2
	v_mfma_f32_16x16x128_f8f6f4 v[208:211], v[122:127], v[50:55], 0 cbsz:2 blgp:2
	v_mfma_f32_16x16x128_f8f6f4 v[212:215], v[122:127], v[62:67], v[188:191] cbsz:2 blgp:2
	s_waitcnt lgkmcnt(0)
	v_mfma_f32_16x16x128_f8f6f4 v[134:137], v[128:133], v[8:13], v[134:137] cbsz:2 blgp:2
	v_mfma_f32_16x16x128_f8f6f4 v[204:207], v[128:133], v[44:49], v[204:207] cbsz:2 blgp:2
	v_mfma_f32_16x16x128_f8f6f4 v[138:141], v[128:133], v[20:25], v[138:141] cbsz:2 blgp:2
	v_mfma_f32_16x16x128_f8f6f4 v[208:211], v[128:133], v[56:61], v[208:211] cbsz:2 blgp:2
	v_mfma_f32_16x16x128_f8f6f4 v[142:145], v[128:133], v[32:37], v[142:145] cbsz:2 blgp:2
	v_mfma_f32_16x16x128_f8f6f4 v[212:215], v[128:133], v[68:73], v[212:215] cbsz:2 blgp:2
	v_cndmask_b32_e64 v158, v134, v204, s[0:1]
	v_cndmask_b32_e64 v159, v138, v208, s[0:1]
	v_fma_mix_f32 v158, v158, v100, v83 op_sel_hi:[0,0,1]
	v_fma_mix_f32 v159, v159, v101, v75 op_sel_hi:[0,0,1]
	v_exp_f32_e32 v158, v158
	v_exp_f32_e32 v159, v159
	v_fma_f32 v158, v158, v186, v186
	v_add_f32_e32 v159, 1.0, v159
	v_rcp_f32_e32 v158, v158
	v_rcp_f32_e32 v159, v159
	v_cndmask_b32_e64 v160, v142, v212, s[0:1]
	v_fma_mix_f32 v161, v158, v160, v79 op_sel_hi:[0,0,1]
	v_exp_f32_e32 v161, v161
	s_add_u32 s48, s48, s40
	v_add_f32_e32 v161, 1.0, v161
	v_rcp_f32_e32 v161, v161
	s_addc_u32 s49, s49, s41
	v_fma_f32 v162, v161, -2.0, 1.0
	v_sub_f32_e32 v163, v176, v162
	v_fma_f32 v176, v159, v163, v162
	v_fma_f32 v164, |v176|, s17, v113
	v_fma_f32 v165, |v176|, s18, v114
	v_fma_f32 v166, |v176|, s19, v115
	v_lshrrev_b32_e32 v167, 26, v176
	v_min3_u32 v164, v164, v165, v166
	v_bfi_b32 v168, 31, v164, v167
	s_nop 1
	v_mul_u32_u24_dpp v170, v168, v180 quad_perm:[1,2,3,3] row_mask:0xf bank_mask:0xf bound_ctrl:1
	v_mad_u32_u24 v171, v168, v181, v170
	ds_write_b8_d16_hi v184, v171 offset:544
	s_barrier
	global_store_short_d16_hi v185, v176, s[48:49]
	s_waitcnt lgkmcnt(0)
	s_barrier
	ds_read_b128 v[122:125], v192 offset:544
	ds_read_b64 v[126:127], v192 offset:560
	ds_read_b128 v[128:131], v192 offset:672
	ds_read_b64 v[132:133], v192 offset:688
	s_nop 7
	s_nop 7
	s_waitcnt lgkmcnt(2)
	v_mfma_f32_16x16x128_f8f6f4 v[134:137], v[122:127], v[2:7], 0 cbsz:2 blgp:2
	v_mfma_f32_16x16x128_f8f6f4 v[138:141], v[122:127], v[14:19], 0 cbsz:2 blgp:2
	v_mfma_f32_16x16x128_f8f6f4 v[142:145], v[122:127], v[26:31], v[188:191] cbsz:2 blgp:2
	v_mfma_f32_16x16x128_f8f6f4 v[204:207], v[122:127], v[38:43], 0 cbsz:2 blgp:2
	v_mfma_f32_16x16x128_f8f6f4 v[208:211], v[122:127], v[50:55], 0 cbsz:2 blgp:2
	v_mfma_f32_16x16x128_f8f6f4 v[212:215], v[122:127], v[62:67], v[188:191] cbsz:2 blgp:2
	s_waitcnt lgkmcnt(0)
	v_mfma_f32_16x16x128_f8f6f4 v[134:137], v[128:133], v[8:13], v[134:137] cbsz:2 blgp:2
	v_mfma_f32_16x16x128_f8f6f4 v[204:207], v[128:133], v[44:49], v[204:207] cbsz:2 blgp:2
	v_mfma_f32_16x16x128_f8f6f4 v[138:141], v[128:133], v[20:25], v[138:141] cbsz:2 blgp:2
	v_mfma_f32_16x16x128_f8f6f4 v[208:211], v[128:133], v[56:61], v[208:211] cbsz:2 blgp:2
	v_mfma_f32_16x16x128_f8f6f4 v[142:145], v[128:133], v[32:37], v[142:145] cbsz:2 blgp:2
	v_mfma_f32_16x16x128_f8f6f4 v[212:215], v[128:133], v[68:73], v[212:215] cbsz:2 blgp:2
	v_cndmask_b32_e64 v158, v134, v204, s[0:1]
	v_cndmask_b32_e64 v159, v138, v208, s[0:1]
	v_fma_mix_f32 v158, v158, v100, v83 op_sel:[0,0,1] op_sel_hi:[0,0,1]
	v_fma_mix_f32 v159, v159, v101, v75 op_sel:[0,0,1] op_sel_hi:[0,0,1]
	v_exp_f32_e32 v158, v158
	v_exp_f32_e32 v159, v159
	v_fma_f32 v158, v158, v186, v186
	v_add_f32_e32 v159, 1.0, v159
	v_rcp_f32_e32 v158, v158
	v_rcp_f32_e32 v159, v159
	v_cndmask_b32_e64 v160, v142, v212, s[0:1]
	v_fma_mix_f32 v161, v158, v160, v79 op_sel:[0,0,1] op_sel_hi:[0,0,1]
	v_exp_f32_e32 v161, v161
	s_add_u32 s48, s48, s40
	v_add_f32_e32 v161, 1.0, v161
	v_rcp_f32_e32 v161, v161
	s_addc_u32 s49, s49, s41
	v_fma_f32 v162, v161, -2.0, 1.0
	v_sub_f32_e32 v163, v176, v162
	v_fma_f32 v176, v159, v163, v162
	v_fma_f32 v164, |v176|, s17, v113
	v_fma_f32 v165, |v176|, s18, v114
	v_fma_f32 v166, |v176|, s19, v115
	v_lshrrev_b32_e32 v167, 26, v176
	v_min3_u32 v164, v164, v165, v166
	v_bfi_b32 v168, 31, v164, v167
	s_nop 1
	v_mul_u32_u24_dpp v170, v168, v180 quad_perm:[1,2,3,3] row_mask:0xf bank_mask:0xf bound_ctrl:1
	v_mad_u32_u24 v171, v168, v181, v170
	ds_write_b8_d16_hi v184, v171
	s_barrier
	global_store_short_d16_hi v185, v176, s[48:49]
	s_waitcnt lgkmcnt(0)
	s_barrier
	ds_read_b128 v[122:125], v192 offset:0
	ds_read_b64 v[126:127], v192 offset:16
	ds_read_b128 v[128:131], v192 offset:128
	ds_read_b64 v[132:133], v192 offset:144
	s_nop 7
	s_nop 7
	s_waitcnt lgkmcnt(2)
	v_mfma_f32_16x16x128_f8f6f4 v[134:137], v[122:127], v[2:7], 0 cbsz:2 blgp:2
	v_mfma_f32_16x16x128_f8f6f4 v[138:141], v[122:127], v[14:19], 0 cbsz:2 blgp:2
	v_mfma_f32_16x16x128_f8f6f4 v[142:145], v[122:127], v[26:31], v[188:191] cbsz:2 blgp:2
	v_mfma_f32_16x16x128_f8f6f4 v[204:207], v[122:127], v[38:43], 0 cbsz:2 blgp:2
	v_mfma_f32_16x16x128_f8f6f4 v[208:211], v[122:127], v[50:55], 0 cbsz:2 blgp:2
	v_mfma_f32_16x16x128_f8f6f4 v[212:215], v[122:127], v[62:67], v[188:191] cbsz:2 blgp:2
	s_waitcnt lgkmcnt(0)
	v_mfma_f32_16x16x128_f8f6f4 v[134:137], v[128:133], v[8:13], v[134:137] cbsz:2 blgp:2
	v_mfma_f32_16x16x128_f8f6f4 v[204:207], v[128:133], v[44:49], v[204:207] cbsz:2 blgp:2
	v_mfma_f32_16x16x128_f8f6f4 v[138:141], v[128:133], v[20:25], v[138:141] cbsz:2 blgp:2
	v_mfma_f32_16x16x128_f8f6f4 v[208:211], v[128:133], v[56:61], v[208:211] cbsz:2 blgp:2
	v_mfma_f32_16x16x128_f8f6f4 v[142:145], v[128:133], v[32:37], v[142:145] cbsz:2 blgp:2
	v_mfma_f32_16x16x128_f8f6f4 v[212:215], v[128:133], v[68:73], v[212:215] cbsz:2 blgp:2
	v_cndmask_b32_e64 v158, v134, v204, s[0:1]
	v_cndmask_b32_e64 v159, v138, v208, s[0:1]
	v_fma_mix_f32 v158, v158, v100, v84 op_sel_hi:[0,0,1]
	v_fma_mix_f32 v159, v159, v101, v76 op_sel_hi:[0,0,1]
	v_exp_f32_e32 v158, v158
	v_exp_f32_e32 v159, v159
	v_fma_f32 v158, v158, v186, v186
	v_add_f32_e32 v159, 1.0, v159
	v_rcp_f32_e32 v158, v158
	v_rcp_f32_e32 v159, v159
	v_cndmask_b32_e64 v160, v142, v212, s[0:1]
	v_fma_mix_f32 v161, v158, v160, v80 op_sel_hi:[0,0,1]
	v_exp_f32_e32 v161, v161
	s_add_u32 s48, s48, s40
	v_add_f32_e32 v161, 1.0, v161
	v_rcp_f32_e32 v161, v161
	s_addc_u32 s49, s49, s41
	v_fma_f32 v162, v161, -2.0, 1.0
	v_sub_f32_e32 v163, v176, v162
	v_fma_f32 v176, v159, v163, v162
	v_fma_f32 v164, |v176|, s17, v113
	v_fma_f32 v165, |v176|, s18, v114
	v_fma_f32 v166, |v176|, s19, v115
	v_lshrrev_b32_e32 v167, 26, v176
	v_min3_u32 v164, v164, v165, v166
	v_bfi_b32 v168, 31, v164, v167
	s_nop 1
	v_mul_u32_u24_dpp v170, v168, v180 quad_perm:[1,2,3,3] row_mask:0xf bank_mask:0xf bound_ctrl:1
	v_mad_u32_u24 v171, v168, v181, v170
	ds_write_b8_d16_hi v184, v171 offset:544
	s_barrier
	global_store_short_d16_hi v185, v176, s[48:49]
	s_waitcnt lgkmcnt(0)
	s_barrier
	ds_read_b128 v[122:125], v192 offset:544
	ds_read_b64 v[126:127], v192 offset:560
	ds_read_b128 v[128:131], v192 offset:672
	ds_read_b64 v[132:133], v192 offset:688
	s_nop 7
	s_nop 7
	s_waitcnt lgkmcnt(2)
	v_mfma_f32_16x16x128_f8f6f4 v[134:137], v[122:127], v[2:7], 0 cbsz:2 blgp:2
	v_mfma_f32_16x16x128_f8f6f4 v[138:141], v[122:127], v[14:19], 0 cbsz:2 blgp:2
	v_mfma_f32_16x16x128_f8f6f4 v[142:145], v[122:127], v[26:31], v[188:191] cbsz:2 blgp:2
	v_mfma_f32_16x16x128_f8f6f4 v[204:207], v[122:127], v[38:43], 0 cbsz:2 blgp:2
	v_mfma_f32_16x16x128_f8f6f4 v[208:211], v[122:127], v[50:55], 0 cbsz:2 blgp:2
	v_mfma_f32_16x16x128_f8f6f4 v[212:215], v[122:127], v[62:67], v[188:191] cbsz:2 blgp:2
	s_waitcnt lgkmcnt(0)
	v_mfma_f32_16x16x128_f8f6f4 v[134:137], v[128:133], v[8:13], v[134:137] cbsz:2 blgp:2
	v_mfma_f32_16x16x128_f8f6f4 v[204:207], v[128:133], v[44:49], v[204:207] cbsz:2 blgp:2
	v_mfma_f32_16x16x128_f8f6f4 v[138:141], v[128:133], v[20:25], v[138:141] cbsz:2 blgp:2
	v_mfma_f32_16x16x128_f8f6f4 v[208:211], v[128:133], v[56:61], v[208:211] cbsz:2 blgp:2
	v_mfma_f32_16x16x128_f8f6f4 v[142:145], v[128:133], v[32:37], v[142:145] cbsz:2 blgp:2
	v_mfma_f32_16x16x128_f8f6f4 v[212:215], v[128:133], v[68:73], v[212:215] cbsz:2 blgp:2
	v_cndmask_b32_e64 v158, v134, v204, s[0:1]
	v_cndmask_b32_e64 v159, v138, v208, s[0:1]
	v_fma_mix_f32 v158, v158, v100, v84 op_sel:[0,0,1] op_sel_hi:[0,0,1]
	v_fma_mix_f32 v159, v159, v101, v76 op_sel:[0,0,1] op_sel_hi:[0,0,1]
	v_exp_f32_e32 v158, v158
	v_exp_f32_e32 v159, v159
	v_fma_f32 v158, v158, v186, v186
	v_add_f32_e32 v159, 1.0, v159
	v_rcp_f32_e32 v158, v158
	v_rcp_f32_e32 v159, v159
	v_cndmask_b32_e64 v160, v142, v212, s[0:1]
	v_fma_mix_f32 v161, v158, v160, v80 op_sel:[0,0,1] op_sel_hi:[0,0,1]
	v_exp_f32_e32 v161, v161
	s_add_u32 s48, s48, s40
	v_add_f32_e32 v161, 1.0, v161
	v_rcp_f32_e32 v161, v161
	s_addc_u32 s49, s49, s41
	v_fma_f32 v162, v161, -2.0, 1.0
	v_sub_f32_e32 v163, v176, v162
	v_fma_f32 v176, v159, v163, v162
	v_fma_f32 v164, |v176|, s17, v113
	v_fma_f32 v165, |v176|, s18, v114
	v_fma_f32 v166, |v176|, s19, v115
	v_lshrrev_b32_e32 v167, 26, v176
	v_min3_u32 v164, v164, v165, v166
	v_bfi_b32 v168, 31, v164, v167
	s_nop 1
	v_mul_u32_u24_dpp v170, v168, v180 quad_perm:[1,2,3,3] row_mask:0xf bank_mask:0xf bound_ctrl:1
	v_mad_u32_u24 v171, v168, v181, v170
	ds_write_b8_d16_hi v184, v171
	s_barrier
	global_store_short_d16_hi v185, v176, s[48:49]
	s_waitcnt lgkmcnt(0)
	s_barrier
	ds_read_b128 v[122:125], v192 offset:0
	ds_read_b64 v[126:127], v192 offset:16
	ds_read_b128 v[128:131], v192 offset:128
	ds_read_b64 v[132:133], v192 offset:144
	s_nop 7
	s_nop 7
	s_waitcnt lgkmcnt(2)
	v_mfma_f32_16x16x128_f8f6f4 v[134:137], v[122:127], v[2:7], 0 cbsz:2 blgp:2
	v_mfma_f32_16x16x128_f8f6f4 v[138:141], v[122:127], v[14:19], 0 cbsz:2 blgp:2
	v_mfma_f32_16x16x128_f8f6f4 v[142:145], v[122:127], v[26:31], v[188:191] cbsz:2 blgp:2
	v_mfma_f32_16x16x128_f8f6f4 v[204:207], v[122:127], v[38:43], 0 cbsz:2 blgp:2
	v_mfma_f32_16x16x128_f8f6f4 v[208:211], v[122:127], v[50:55], 0 cbsz:2 blgp:2
	v_mfma_f32_16x16x128_f8f6f4 v[212:215], v[122:127], v[62:67], v[188:191] cbsz:2 blgp:2
	s_waitcnt lgkmcnt(0)
	v_mfma_f32_16x16x128_f8f6f4 v[134:137], v[128:133], v[8:13], v[134:137] cbsz:2 blgp:2
	v_mfma_f32_16x16x128_f8f6f4 v[204:207], v[128:133], v[44:49], v[204:207] cbsz:2 blgp:2
	v_mfma_f32_16x16x128_f8f6f4 v[138:141], v[128:133], v[20:25], v[138:141] cbsz:2 blgp:2
	v_mfma_f32_16x16x128_f8f6f4 v[208:211], v[128:133], v[56:61], v[208:211] cbsz:2 blgp:2
	v_mfma_f32_16x16x128_f8f6f4 v[142:145], v[128:133], v[32:37], v[142:145] cbsz:2 blgp:2
	v_mfma_f32_16x16x128_f8f6f4 v[212:215], v[128:133], v[68:73], v[212:215] cbsz:2 blgp:2
	v_cndmask_b32_e64 v158, v134, v204, s[0:1]
	v_cndmask_b32_e64 v159, v138, v208, s[0:1]
	v_fma_mix_f32 v158, v158, v100, v85 op_sel_hi:[0,0,1]
	v_fma_mix_f32 v159, v159, v101, v77 op_sel_hi:[0,0,1]
	v_exp_f32_e32 v158, v158
	v_exp_f32_e32 v159, v159
	v_fma_f32 v158, v158, v186, v186
	v_add_f32_e32 v159, 1.0, v159
	v_rcp_f32_e32 v158, v158
	v_rcp_f32_e32 v159, v159
	v_cndmask_b32_e64 v160, v142, v212, s[0:1]
	v_fma_mix_f32 v161, v158, v160, v81 op_sel_hi:[0,0,1]
	v_exp_f32_e32 v161, v161
	s_add_u32 s48, s48, s40
	v_add_f32_e32 v161, 1.0, v161
	v_rcp_f32_e32 v161, v161
	s_addc_u32 s49, s49, s41
	v_fma_f32 v162, v161, -2.0, 1.0
	v_sub_f32_e32 v163, v176, v162
	v_fma_f32 v176, v159, v163, v162
	v_fma_f32 v164, |v176|, s17, v113
	v_fma_f32 v165, |v176|, s18, v114
	v_fma_f32 v166, |v176|, s19, v115
	v_lshrrev_b32_e32 v167, 26, v176
	v_min3_u32 v164, v164, v165, v166
	v_bfi_b32 v168, 31, v164, v167
	s_nop 1
	v_mul_u32_u24_dpp v170, v168, v180 quad_perm:[1,2,3,3] row_mask:0xf bank_mask:0xf bound_ctrl:1
	v_mad_u32_u24 v171, v168, v181, v170
	ds_write_b8_d16_hi v184, v171 offset:544
	s_barrier
	global_store_short_d16_hi v185, v176, s[48:49]
	s_waitcnt lgkmcnt(0)
	s_barrier
	ds_read_b128 v[122:125], v192 offset:544
	ds_read_b64 v[126:127], v192 offset:560
	ds_read_b128 v[128:131], v192 offset:672
	ds_read_b64 v[132:133], v192 offset:688
	s_nop 7
	s_nop 7
	s_waitcnt lgkmcnt(2)
	v_mfma_f32_16x16x128_f8f6f4 v[134:137], v[122:127], v[2:7], 0 cbsz:2 blgp:2
	v_mfma_f32_16x16x128_f8f6f4 v[138:141], v[122:127], v[14:19], 0 cbsz:2 blgp:2
	v_mfma_f32_16x16x128_f8f6f4 v[142:145], v[122:127], v[26:31], v[188:191] cbsz:2 blgp:2
	v_mfma_f32_16x16x128_f8f6f4 v[204:207], v[122:127], v[38:43], 0 cbsz:2 blgp:2
	v_mfma_f32_16x16x128_f8f6f4 v[208:211], v[122:127], v[50:55], 0 cbsz:2 blgp:2
	v_mfma_f32_16x16x128_f8f6f4 v[212:215], v[122:127], v[62:67], v[188:191] cbsz:2 blgp:2
	s_waitcnt lgkmcnt(0)
	v_mfma_f32_16x16x128_f8f6f4 v[134:137], v[128:133], v[8:13], v[134:137] cbsz:2 blgp:2
	v_mfma_f32_16x16x128_f8f6f4 v[204:207], v[128:133], v[44:49], v[204:207] cbsz:2 blgp:2
	v_mfma_f32_16x16x128_f8f6f4 v[138:141], v[128:133], v[20:25], v[138:141] cbsz:2 blgp:2
	v_mfma_f32_16x16x128_f8f6f4 v[208:211], v[128:133], v[56:61], v[208:211] cbsz:2 blgp:2
	v_mfma_f32_16x16x128_f8f6f4 v[142:145], v[128:133], v[32:37], v[142:145] cbsz:2 blgp:2
	v_mfma_f32_16x16x128_f8f6f4 v[212:215], v[128:133], v[68:73], v[212:215] cbsz:2 blgp:2
	v_cndmask_b32_e64 v158, v134, v204, s[0:1]
	v_cndmask_b32_e64 v159, v138, v208, s[0:1]
	v_fma_mix_f32 v158, v158, v100, v85 op_sel:[0,0,1] op_sel_hi:[0,0,1]
	v_fma_mix_f32 v159, v159, v101, v77 op_sel:[0,0,1] op_sel_hi:[0,0,1]
	v_exp_f32_e32 v158, v158
	v_exp_f32_e32 v159, v159
	v_fma_f32 v158, v158, v186, v186
	v_add_f32_e32 v159, 1.0, v159
	v_rcp_f32_e32 v158, v158
	v_rcp_f32_e32 v159, v159
	v_cndmask_b32_e64 v160, v142, v212, s[0:1]
	v_fma_mix_f32 v161, v158, v160, v81 op_sel:[0,0,1] op_sel_hi:[0,0,1]
	v_exp_f32_e32 v161, v161
	s_add_u32 s48, s48, s40
	v_add_f32_e32 v161, 1.0, v161
	v_rcp_f32_e32 v161, v161
	s_addc_u32 s49, s49, s41
	v_fma_f32 v162, v161, -2.0, 1.0
	v_sub_f32_e32 v163, v176, v162
	v_fma_f32 v176, v159, v163, v162
	v_fma_f32 v164, |v176|, s17, v113
	v_fma_f32 v165, |v176|, s18, v114
	v_fma_f32 v166, |v176|, s19, v115
	v_lshrrev_b32_e32 v167, 26, v176
	v_min3_u32 v164, v164, v165, v166
	v_bfi_b32 v168, 31, v164, v167
	s_nop 1
	v_mul_u32_u24_dpp v170, v168, v180 quad_perm:[1,2,3,3] row_mask:0xf bank_mask:0xf bound_ctrl:1
	v_mad_u32_u24 v171, v168, v181, v170
	ds_write_b8_d16_hi v184, v171
	s_barrier
	global_store_short_d16_hi v185, v176, s[48:49]
	s_waitcnt lgkmcnt(0)
	s_barrier
	ds_read_b128 v[122:125], v192 offset:0
	ds_read_b64 v[126:127], v192 offset:16
	ds_read_b128 v[128:131], v192 offset:128
	ds_read_b64 v[132:133], v192 offset:144
	s_waitcnt vmcnt(8)
	global_load_dwordx4 v[82:85], v[196:197], off
	global_load_dwordx4 v[74:77], v[196:197], off offset:512
	global_load_dwordx4 v[78:81], v[196:197], off offset:1024
	v_lshl_add_u64 v[196:197], v[196:197], 0, s[42:43]
	s_nop 7
	s_nop 7
	s_waitcnt lgkmcnt(2)
	v_mfma_f32_16x16x128_f8f6f4 v[134:137], v[122:127], v[2:7], 0 cbsz:2 blgp:2
	v_mfma_f32_16x16x128_f8f6f4 v[138:141], v[122:127], v[14:19], 0 cbsz:2 blgp:2
	v_mfma_f32_16x16x128_f8f6f4 v[142:145], v[122:127], v[26:31], v[188:191] cbsz:2 blgp:2
	v_mfma_f32_16x16x128_f8f6f4 v[204:207], v[122:127], v[38:43], 0 cbsz:2 blgp:2
	v_mfma_f32_16x16x128_f8f6f4 v[208:211], v[122:127], v[50:55], 0 cbsz:2 blgp:2
	v_mfma_f32_16x16x128_f8f6f4 v[212:215], v[122:127], v[62:67], v[188:191] cbsz:2 blgp:2
	s_waitcnt lgkmcnt(0)
	v_mfma_f32_16x16x128_f8f6f4 v[134:137], v[128:133], v[8:13], v[134:137] cbsz:2 blgp:2
	v_mfma_f32_16x16x128_f8f6f4 v[204:207], v[128:133], v[44:49], v[204:207] cbsz:2 blgp:2
	v_mfma_f32_16x16x128_f8f6f4 v[138:141], v[128:133], v[20:25], v[138:141] cbsz:2 blgp:2
	v_mfma_f32_16x16x128_f8f6f4 v[208:211], v[128:133], v[56:61], v[208:211] cbsz:2 blgp:2
	v_mfma_f32_16x16x128_f8f6f4 v[142:145], v[128:133], v[32:37], v[142:145] cbsz:2 blgp:2
	v_mfma_f32_16x16x128_f8f6f4 v[212:215], v[128:133], v[68:73], v[212:215] cbsz:2 blgp:2
	v_cndmask_b32_e64 v158, v134, v204, s[0:1]
	v_cndmask_b32_e64 v159, v138, v208, s[0:1]
	v_fma_mix_f32 v158, v158, v100, v146 op_sel_hi:[0,0,1]
	v_fma_mix_f32 v159, v159, v101, v150 op_sel_hi:[0,0,1]
	v_exp_f32_e32 v158, v158
	v_exp_f32_e32 v159, v159
	v_fma_f32 v158, v158, v186, v186
	v_add_f32_e32 v159, 1.0, v159
	v_rcp_f32_e32 v158, v158
	v_rcp_f32_e32 v159, v159
	v_cndmask_b32_e64 v160, v142, v212, s[0:1]
	v_fma_mix_f32 v161, v158, v160, v154 op_sel_hi:[0,0,1]
	v_exp_f32_e32 v161, v161
	s_add_u32 s48, s48, s40
	v_add_f32_e32 v161, 1.0, v161
	v_rcp_f32_e32 v161, v161
	s_addc_u32 s49, s49, s41
	v_fma_f32 v162, v161, -2.0, 1.0
	v_sub_f32_e32 v163, v176, v162
	v_fma_f32 v176, v159, v163, v162
	v_fma_f32 v164, |v176|, s17, v113
	v_fma_f32 v165, |v176|, s18, v114
	v_fma_f32 v166, |v176|, s19, v115
	v_lshrrev_b32_e32 v167, 26, v176
	v_min3_u32 v164, v164, v165, v166
	v_bfi_b32 v168, 31, v164, v167
	s_nop 1
	v_mul_u32_u24_dpp v170, v168, v180 quad_perm:[1,2,3,3] row_mask:0xf bank_mask:0xf bound_ctrl:1
	v_mad_u32_u24 v171, v168, v181, v170
	ds_write_b8_d16_hi v184, v171 offset:544
	s_barrier
	global_store_short_d16_hi v185, v176, s[48:49]
	s_waitcnt lgkmcnt(0)
	s_barrier
	ds_read_b128 v[122:125], v192 offset:544
	ds_read_b64 v[126:127], v192 offset:560
	ds_read_b128 v[128:131], v192 offset:672
	ds_read_b64 v[132:133], v192 offset:688
	s_nop 7
	s_nop 7
	s_waitcnt lgkmcnt(2)
	v_mfma_f32_16x16x128_f8f6f4 v[134:137], v[122:127], v[2:7], 0 cbsz:2 blgp:2
	v_mfma_f32_16x16x128_f8f6f4 v[138:141], v[122:127], v[14:19], 0 cbsz:2 blgp:2
	v_mfma_f32_16x16x128_f8f6f4 v[142:145], v[122:127], v[26:31], v[188:191] cbsz:2 blgp:2
	v_mfma_f32_16x16x128_f8f6f4 v[204:207], v[122:127], v[38:43], 0 cbsz:2 blgp:2
	v_mfma_f32_16x16x128_f8f6f4 v[208:211], v[122:127], v[50:55], 0 cbsz:2 blgp:2
	v_mfma_f32_16x16x128_f8f6f4 v[212:215], v[122:127], v[62:67], v[188:191] cbsz:2 blgp:2
	s_waitcnt lgkmcnt(0)
	v_mfma_f32_16x16x128_f8f6f4 v[134:137], v[128:133], v[8:13], v[134:137] cbsz:2 blgp:2
	v_mfma_f32_16x16x128_f8f6f4 v[204:207], v[128:133], v[44:49], v[204:207] cbsz:2 blgp:2
	v_mfma_f32_16x16x128_f8f6f4 v[138:141], v[128:133], v[20:25], v[138:141] cbsz:2 blgp:2
	v_mfma_f32_16x16x128_f8f6f4 v[208:211], v[128:133], v[56:61], v[208:211] cbsz:2 blgp:2
	v_mfma_f32_16x16x128_f8f6f4 v[142:145], v[128:133], v[32:37], v[142:145] cbsz:2 blgp:2
	v_mfma_f32_16x16x128_f8f6f4 v[212:215], v[128:133], v[68:73], v[212:215] cbsz:2 blgp:2
	v_cndmask_b32_e64 v158, v134, v204, s[0:1]
	v_cndmask_b32_e64 v159, v138, v208, s[0:1]
	v_fma_mix_f32 v158, v158, v100, v146 op_sel:[0,0,1] op_sel_hi:[0,0,1]
	v_fma_mix_f32 v159, v159, v101, v150 op_sel:[0,0,1] op_sel_hi:[0,0,1]
	v_exp_f32_e32 v158, v158
	v_exp_f32_e32 v159, v159
	v_fma_f32 v158, v158, v186, v186
	v_add_f32_e32 v159, 1.0, v159
	v_rcp_f32_e32 v158, v158
	v_rcp_f32_e32 v159, v159
	v_cndmask_b32_e64 v160, v142, v212, s[0:1]
	v_fma_mix_f32 v161, v158, v160, v154 op_sel:[0,0,1] op_sel_hi:[0,0,1]
	v_exp_f32_e32 v161, v161
	s_add_u32 s48, s48, s40
	v_add_f32_e32 v161, 1.0, v161
	v_rcp_f32_e32 v161, v161
	s_addc_u32 s49, s49, s41
	v_fma_f32 v162, v161, -2.0, 1.0
	v_sub_f32_e32 v163, v176, v162
	v_fma_f32 v176, v159, v163, v162
	v_fma_f32 v164, |v176|, s17, v113
	v_fma_f32 v165, |v176|, s18, v114
	v_fma_f32 v166, |v176|, s19, v115
	v_lshrrev_b32_e32 v167, 26, v176
	v_min3_u32 v164, v164, v165, v166
	v_bfi_b32 v168, 31, v164, v167
	s_nop 1
	v_mul_u32_u24_dpp v170, v168, v180 quad_perm:[1,2,3,3] row_mask:0xf bank_mask:0xf bound_ctrl:1
	v_mad_u32_u24 v171, v168, v181, v170
	ds_write_b8_d16_hi v184, v171
	s_barrier
	global_store_short_d16_hi v185, v176, s[48:49]
	s_waitcnt lgkmcnt(0)
	s_barrier
	ds_read_b128 v[122:125], v192 offset:0
	ds_read_b64 v[126:127], v192 offset:16
	ds_read_b128 v[128:131], v192 offset:128
	ds_read_b64 v[132:133], v192 offset:144
	s_nop 7
	s_nop 7
	s_waitcnt lgkmcnt(2)
	v_mfma_f32_16x16x128_f8f6f4 v[134:137], v[122:127], v[2:7], 0 cbsz:2 blgp:2
	v_mfma_f32_16x16x128_f8f6f4 v[138:141], v[122:127], v[14:19], 0 cbsz:2 blgp:2
	v_mfma_f32_16x16x128_f8f6f4 v[142:145], v[122:127], v[26:31], v[188:191] cbsz:2 blgp:2
	v_mfma_f32_16x16x128_f8f6f4 v[204:207], v[122:127], v[38:43], 0 cbsz:2 blgp:2
	v_mfma_f32_16x16x128_f8f6f4 v[208:211], v[122:127], v[50:55], 0 cbsz:2 blgp:2
	v_mfma_f32_16x16x128_f8f6f4 v[212:215], v[122:127], v[62:67], v[188:191] cbsz:2 blgp:2
	s_waitcnt lgkmcnt(0)
	v_mfma_f32_16x16x128_f8f6f4 v[134:137], v[128:133], v[8:13], v[134:137] cbsz:2 blgp:2
	v_mfma_f32_16x16x128_f8f6f4 v[204:207], v[128:133], v[44:49], v[204:207] cbsz:2 blgp:2
	v_mfma_f32_16x16x128_f8f6f4 v[138:141], v[128:133], v[20:25], v[138:141] cbsz:2 blgp:2
	v_mfma_f32_16x16x128_f8f6f4 v[208:211], v[128:133], v[56:61], v[208:211] cbsz:2 blgp:2
	v_mfma_f32_16x16x128_f8f6f4 v[142:145], v[128:133], v[32:37], v[142:145] cbsz:2 blgp:2
	v_mfma_f32_16x16x128_f8f6f4 v[212:215], v[128:133], v[68:73], v[212:215] cbsz:2 blgp:2
	v_cndmask_b32_e64 v158, v134, v204, s[0:1]
	v_cndmask_b32_e64 v159, v138, v208, s[0:1]
	v_fma_mix_f32 v158, v158, v100, v147 op_sel_hi:[0,0,1]
	v_fma_mix_f32 v159, v159, v101, v151 op_sel_hi:[0,0,1]
	v_exp_f32_e32 v158, v158
	v_exp_f32_e32 v159, v159
	v_fma_f32 v158, v158, v186, v186
	v_add_f32_e32 v159, 1.0, v159
	v_rcp_f32_e32 v158, v158
	v_rcp_f32_e32 v159, v159
	v_cndmask_b32_e64 v160, v142, v212, s[0:1]
	v_fma_mix_f32 v161, v158, v160, v155 op_sel_hi:[0,0,1]
	v_exp_f32_e32 v161, v161
	s_add_u32 s48, s48, s40
	v_add_f32_e32 v161, 1.0, v161
	v_rcp_f32_e32 v161, v161
	s_addc_u32 s49, s49, s41
	v_fma_f32 v162, v161, -2.0, 1.0
	v_sub_f32_e32 v163, v176, v162
	v_fma_f32 v176, v159, v163, v162
	v_fma_f32 v164, |v176|, s17, v113
	v_fma_f32 v165, |v176|, s18, v114
	v_fma_f32 v166, |v176|, s19, v115
	v_lshrrev_b32_e32 v167, 26, v176
	v_min3_u32 v164, v164, v165, v166
	v_bfi_b32 v168, 31, v164, v167
	s_nop 1
	v_mul_u32_u24_dpp v170, v168, v180 quad_perm:[1,2,3,3] row_mask:0xf bank_mask:0xf bound_ctrl:1
	v_mad_u32_u24 v171, v168, v181, v170
	ds_write_b8_d16_hi v184, v171 offset:544
	s_barrier
	global_store_short_d16_hi v185, v176, s[48:49]
	s_waitcnt lgkmcnt(0)
	s_barrier
	ds_read_b128 v[122:125], v192 offset:544
	ds_read_b64 v[126:127], v192 offset:560
	ds_read_b128 v[128:131], v192 offset:672
	ds_read_b64 v[132:133], v192 offset:688
	s_nop 7
	s_nop 7
	s_waitcnt lgkmcnt(2)
	v_mfma_f32_16x16x128_f8f6f4 v[134:137], v[122:127], v[2:7], 0 cbsz:2 blgp:2
	v_mfma_f32_16x16x128_f8f6f4 v[138:141], v[122:127], v[14:19], 0 cbsz:2 blgp:2
	v_mfma_f32_16x16x128_f8f6f4 v[142:145], v[122:127], v[26:31], v[188:191] cbsz:2 blgp:2
	v_mfma_f32_16x16x128_f8f6f4 v[204:207], v[122:127], v[38:43], 0 cbsz:2 blgp:2
	v_mfma_f32_16x16x128_f8f6f4 v[208:211], v[122:127], v[50:55], 0 cbsz:2 blgp:2
	v_mfma_f32_16x16x128_f8f6f4 v[212:215], v[122:127], v[62:67], v[188:191] cbsz:2 blgp:2
	s_waitcnt lgkmcnt(0)
	v_mfma_f32_16x16x128_f8f6f4 v[134:137], v[128:133], v[8:13], v[134:137] cbsz:2 blgp:2
	v_mfma_f32_16x16x128_f8f6f4 v[204:207], v[128:133], v[44:49], v[204:207] cbsz:2 blgp:2
	v_mfma_f32_16x16x128_f8f6f4 v[138:141], v[128:133], v[20:25], v[138:141] cbsz:2 blgp:2
	v_mfma_f32_16x16x128_f8f6f4 v[208:211], v[128:133], v[56:61], v[208:211] cbsz:2 blgp:2
	v_mfma_f32_16x16x128_f8f6f4 v[142:145], v[128:133], v[32:37], v[142:145] cbsz:2 blgp:2
	v_mfma_f32_16x16x128_f8f6f4 v[212:215], v[128:133], v[68:73], v[212:215] cbsz:2 blgp:2
	v_cndmask_b32_e64 v158, v134, v204, s[0:1]
	v_cndmask_b32_e64 v159, v138, v208, s[0:1]
	v_fma_mix_f32 v158, v158, v100, v147 op_sel:[0,0,1] op_sel_hi:[0,0,1]
	v_fma_mix_f32 v159, v159, v101, v151 op_sel:[0,0,1] op_sel_hi:[0,0,1]
	v_exp_f32_e32 v158, v158
	v_exp_f32_e32 v159, v159
	v_fma_f32 v158, v158, v186, v186
	v_add_f32_e32 v159, 1.0, v159
	v_rcp_f32_e32 v158, v158
	v_rcp_f32_e32 v159, v159
	v_cndmask_b32_e64 v160, v142, v212, s[0:1]
	v_fma_mix_f32 v161, v158, v160, v155 op_sel:[0,0,1] op_sel_hi:[0,0,1]
	v_exp_f32_e32 v161, v161
	s_add_u32 s48, s48, s40
	v_add_f32_e32 v161, 1.0, v161
	v_rcp_f32_e32 v161, v161
	s_addc_u32 s49, s49, s41
	v_fma_f32 v162, v161, -2.0, 1.0
	v_sub_f32_e32 v163, v176, v162
	v_fma_f32 v176, v159, v163, v162
	v_fma_f32 v164, |v176|, s17, v113
	v_fma_f32 v165, |v176|, s18, v114
	v_fma_f32 v166, |v176|, s19, v115
	v_lshrrev_b32_e32 v167, 26, v176
	v_min3_u32 v164, v164, v165, v166
	v_bfi_b32 v168, 31, v164, v167
	s_nop 1
	v_mul_u32_u24_dpp v170, v168, v180 quad_perm:[1,2,3,3] row_mask:0xf bank_mask:0xf bound_ctrl:1
	v_mad_u32_u24 v171, v168, v181, v170
	ds_write_b8_d16_hi v184, v171
	s_barrier
	global_store_short_d16_hi v185, v176, s[48:49]
	s_waitcnt lgkmcnt(0)
	s_barrier
	ds_read_b128 v[122:125], v192 offset:0
	ds_read_b64 v[126:127], v192 offset:16
	ds_read_b128 v[128:131], v192 offset:128
	ds_read_b64 v[132:133], v192 offset:144
	s_nop 7
	s_nop 7
	s_waitcnt lgkmcnt(2)
	v_mfma_f32_16x16x128_f8f6f4 v[134:137], v[122:127], v[2:7], 0 cbsz:2 blgp:2
	v_mfma_f32_16x16x128_f8f6f4 v[138:141], v[122:127], v[14:19], 0 cbsz:2 blgp:2
	v_mfma_f32_16x16x128_f8f6f4 v[142:145], v[122:127], v[26:31], v[188:191] cbsz:2 blgp:2
	v_mfma_f32_16x16x128_f8f6f4 v[204:207], v[122:127], v[38:43], 0 cbsz:2 blgp:2
	v_mfma_f32_16x16x128_f8f6f4 v[208:211], v[122:127], v[50:55], 0 cbsz:2 blgp:2
	v_mfma_f32_16x16x128_f8f6f4 v[212:215], v[122:127], v[62:67], v[188:191] cbsz:2 blgp:2
	s_waitcnt lgkmcnt(0)
	v_mfma_f32_16x16x128_f8f6f4 v[134:137], v[128:133], v[8:13], v[134:137] cbsz:2 blgp:2
	v_mfma_f32_16x16x128_f8f6f4 v[204:207], v[128:133], v[44:49], v[204:207] cbsz:2 blgp:2
	v_mfma_f32_16x16x128_f8f6f4 v[138:141], v[128:133], v[20:25], v[138:141] cbsz:2 blgp:2
	v_mfma_f32_16x16x128_f8f6f4 v[208:211], v[128:133], v[56:61], v[208:211] cbsz:2 blgp:2
	v_mfma_f32_16x16x128_f8f6f4 v[142:145], v[128:133], v[32:37], v[142:145] cbsz:2 blgp:2
	v_mfma_f32_16x16x128_f8f6f4 v[212:215], v[128:133], v[68:73], v[212:215] cbsz:2 blgp:2
	v_cndmask_b32_e64 v158, v134, v204, s[0:1]
	v_cndmask_b32_e64 v159, v138, v208, s[0:1]
	v_fma_mix_f32 v158, v158, v100, v148 op_sel_hi:[0,0,1]
	v_fma_mix_f32 v159, v159, v101, v152 op_sel_hi:[0,0,1]
	v_exp_f32_e32 v158, v158
	v_exp_f32_e32 v159, v159
	v_fma_f32 v158, v158, v186, v186
	v_add_f32_e32 v159, 1.0, v159
	v_rcp_f32_e32 v158, v158
	v_rcp_f32_e32 v159, v159
	v_cndmask_b32_e64 v160, v142, v212, s[0:1]
	v_fma_mix_f32 v161, v158, v160, v156 op_sel_hi:[0,0,1]
	v_exp_f32_e32 v161, v161
	s_add_u32 s48, s48, s40
	v_add_f32_e32 v161, 1.0, v161
	v_rcp_f32_e32 v161, v161
	s_addc_u32 s49, s49, s41
	v_fma_f32 v162, v161, -2.0, 1.0
	v_sub_f32_e32 v163, v176, v162
	v_fma_f32 v176, v159, v163, v162
	v_fma_f32 v164, |v176|, s17, v113
	v_fma_f32 v165, |v176|, s18, v114
	v_fma_f32 v166, |v176|, s19, v115
	v_lshrrev_b32_e32 v167, 26, v176
	v_min3_u32 v164, v164, v165, v166
	v_bfi_b32 v168, 31, v164, v167
	s_nop 1
	v_mul_u32_u24_dpp v170, v168, v180 quad_perm:[1,2,3,3] row_mask:0xf bank_mask:0xf bound_ctrl:1
	v_mad_u32_u24 v171, v168, v181, v170
	ds_write_b8_d16_hi v184, v171 offset:544
	s_barrier
	global_store_short_d16_hi v185, v176, s[48:49]
	s_waitcnt lgkmcnt(0)
	s_barrier
	ds_read_b128 v[122:125], v192 offset:544
	ds_read_b64 v[126:127], v192 offset:560
	ds_read_b128 v[128:131], v192 offset:672
	ds_read_b64 v[132:133], v192 offset:688
	s_nop 7
	s_nop 7
	s_waitcnt lgkmcnt(2)
	v_mfma_f32_16x16x128_f8f6f4 v[134:137], v[122:127], v[2:7], 0 cbsz:2 blgp:2
	v_mfma_f32_16x16x128_f8f6f4 v[138:141], v[122:127], v[14:19], 0 cbsz:2 blgp:2
	v_mfma_f32_16x16x128_f8f6f4 v[142:145], v[122:127], v[26:31], v[188:191] cbsz:2 blgp:2
	v_mfma_f32_16x16x128_f8f6f4 v[204:207], v[122:127], v[38:43], 0 cbsz:2 blgp:2
	v_mfma_f32_16x16x128_f8f6f4 v[208:211], v[122:127], v[50:55], 0 cbsz:2 blgp:2
	v_mfma_f32_16x16x128_f8f6f4 v[212:215], v[122:127], v[62:67], v[188:191] cbsz:2 blgp:2
	s_waitcnt lgkmcnt(0)
	v_mfma_f32_16x16x128_f8f6f4 v[134:137], v[128:133], v[8:13], v[134:137] cbsz:2 blgp:2
	v_mfma_f32_16x16x128_f8f6f4 v[204:207], v[128:133], v[44:49], v[204:207] cbsz:2 blgp:2
	v_mfma_f32_16x16x128_f8f6f4 v[138:141], v[128:133], v[20:25], v[138:141] cbsz:2 blgp:2
	v_mfma_f32_16x16x128_f8f6f4 v[208:211], v[128:133], v[56:61], v[208:211] cbsz:2 blgp:2
	v_mfma_f32_16x16x128_f8f6f4 v[142:145], v[128:133], v[32:37], v[142:145] cbsz:2 blgp:2
	v_mfma_f32_16x16x128_f8f6f4 v[212:215], v[128:133], v[68:73], v[212:215] cbsz:2 blgp:2
	v_cndmask_b32_e64 v158, v134, v204, s[0:1]
	v_cndmask_b32_e64 v159, v138, v208, s[0:1]
	v_fma_mix_f32 v158, v158, v100, v148 op_sel:[0,0,1] op_sel_hi:[0,0,1]
	v_fma_mix_f32 v159, v159, v101, v152 op_sel:[0,0,1] op_sel_hi:[0,0,1]
	v_exp_f32_e32 v158, v158
	v_exp_f32_e32 v159, v159
	v_fma_f32 v158, v158, v186, v186
	v_add_f32_e32 v159, 1.0, v159
	v_rcp_f32_e32 v158, v158
	v_rcp_f32_e32 v159, v159
	v_cndmask_b32_e64 v160, v142, v212, s[0:1]
	v_fma_mix_f32 v161, v158, v160, v156 op_sel:[0,0,1] op_sel_hi:[0,0,1]
	v_exp_f32_e32 v161, v161
	s_add_u32 s48, s48, s40
	v_add_f32_e32 v161, 1.0, v161
	v_rcp_f32_e32 v161, v161
	s_addc_u32 s49, s49, s41
	v_fma_f32 v162, v161, -2.0, 1.0
	v_sub_f32_e32 v163, v176, v162
	v_fma_f32 v176, v159, v163, v162
	v_fma_f32 v164, |v176|, s17, v113
	v_fma_f32 v165, |v176|, s18, v114
	v_fma_f32 v166, |v176|, s19, v115
	v_lshrrev_b32_e32 v167, 26, v176
	v_min3_u32 v164, v164, v165, v166
	v_bfi_b32 v168, 31, v164, v167
	s_nop 1
	v_mul_u32_u24_dpp v170, v168, v180 quad_perm:[1,2,3,3] row_mask:0xf bank_mask:0xf bound_ctrl:1
	v_mad_u32_u24 v171, v168, v181, v170
	ds_write_b8_d16_hi v184, v171
	s_barrier
	global_store_short_d16_hi v185, v176, s[48:49]
	s_waitcnt lgkmcnt(0)
	s_barrier
	ds_read_b128 v[122:125], v192 offset:0
	ds_read_b64 v[126:127], v192 offset:16
	ds_read_b128 v[128:131], v192 offset:128
	ds_read_b64 v[132:133], v192 offset:144
	s_nop 7
	s_nop 7
	s_waitcnt lgkmcnt(2)
	v_mfma_f32_16x16x128_f8f6f4 v[134:137], v[122:127], v[2:7], 0 cbsz:2 blgp:2
	v_mfma_f32_16x16x128_f8f6f4 v[138:141], v[122:127], v[14:19], 0 cbsz:2 blgp:2
	v_mfma_f32_16x16x128_f8f6f4 v[142:145], v[122:127], v[26:31], v[188:191] cbsz:2 blgp:2
	v_mfma_f32_16x16x128_f8f6f4 v[204:207], v[122:127], v[38:43], 0 cbsz:2 blgp:2
	v_mfma_f32_16x16x128_f8f6f4 v[208:211], v[122:127], v[50:55], 0 cbsz:2 blgp:2
	v_mfma_f32_16x16x128_f8f6f4 v[212:215], v[122:127], v[62:67], v[188:191] cbsz:2 blgp:2
	s_waitcnt lgkmcnt(0)
	v_mfma_f32_16x16x128_f8f6f4 v[134:137], v[128:133], v[8:13], v[134:137] cbsz:2 blgp:2
	v_mfma_f32_16x16x128_f8f6f4 v[204:207], v[128:133], v[44:49], v[204:207] cbsz:2 blgp:2
	v_mfma_f32_16x16x128_f8f6f4 v[138:141], v[128:133], v[20:25], v[138:141] cbsz:2 blgp:2
	v_mfma_f32_16x16x128_f8f6f4 v[208:211], v[128:133], v[56:61], v[208:211] cbsz:2 blgp:2
	v_mfma_f32_16x16x128_f8f6f4 v[142:145], v[128:133], v[32:37], v[142:145] cbsz:2 blgp:2
	v_mfma_f32_16x16x128_f8f6f4 v[212:215], v[128:133], v[68:73], v[212:215] cbsz:2 blgp:2
	v_cndmask_b32_e64 v158, v134, v204, s[0:1]
	v_cndmask_b32_e64 v159, v138, v208, s[0:1]
	v_fma_mix_f32 v158, v158, v100, v149 op_sel_hi:[0,0,1]
	v_fma_mix_f32 v159, v159, v101, v153 op_sel_hi:[0,0,1]
	v_exp_f32_e32 v158, v158
	v_exp_f32_e32 v159, v159
	v_fma_f32 v158, v158, v186, v186
	v_add_f32_e32 v159, 1.0, v159
	v_rcp_f32_e32 v158, v158
	v_rcp_f32_e32 v159, v159
	v_cndmask_b32_e64 v160, v142, v212, s[0:1]
	v_fma_mix_f32 v161, v158, v160, v157 op_sel_hi:[0,0,1]
	v_exp_f32_e32 v161, v161
	s_add_u32 s48, s48, s40
	v_add_f32_e32 v161, 1.0, v161
	v_rcp_f32_e32 v161, v161
	s_addc_u32 s49, s49, s41
	v_fma_f32 v162, v161, -2.0, 1.0
	v_sub_f32_e32 v163, v176, v162
	v_fma_f32 v176, v159, v163, v162
	v_fma_f32 v164, |v176|, s17, v113
	v_fma_f32 v165, |v176|, s18, v114
	v_fma_f32 v166, |v176|, s19, v115
	v_lshrrev_b32_e32 v167, 26, v176
	v_min3_u32 v164, v164, v165, v166
	v_bfi_b32 v168, 31, v164, v167
	s_nop 1
	v_mul_u32_u24_dpp v170, v168, v180 quad_perm:[1,2,3,3] row_mask:0xf bank_mask:0xf bound_ctrl:1
	v_mad_u32_u24 v171, v168, v181, v170
	ds_write_b8_d16_hi v184, v171 offset:544
	s_barrier
	global_store_short_d16_hi v185, v176, s[48:49]
	s_waitcnt lgkmcnt(0)
	s_barrier
	ds_read_b128 v[122:125], v192 offset:544
	ds_read_b64 v[126:127], v192 offset:560
	ds_read_b128 v[128:131], v192 offset:672
	ds_read_b64 v[132:133], v192 offset:688
	s_add_i32 s44, s44, 16
	s_nop 7
	s_nop 7
	s_waitcnt lgkmcnt(2)
	v_mfma_f32_16x16x128_f8f6f4 v[134:137], v[122:127], v[2:7], 0 cbsz:2 blgp:2
	v_mfma_f32_16x16x128_f8f6f4 v[138:141], v[122:127], v[14:19], 0 cbsz:2 blgp:2
	v_mfma_f32_16x16x128_f8f6f4 v[142:145], v[122:127], v[26:31], v[188:191] cbsz:2 blgp:2
	v_mfma_f32_16x16x128_f8f6f4 v[204:207], v[122:127], v[38:43], 0 cbsz:2 blgp:2
	v_mfma_f32_16x16x128_f8f6f4 v[208:211], v[122:127], v[50:55], 0 cbsz:2 blgp:2
	v_mfma_f32_16x16x128_f8f6f4 v[212:215], v[122:127], v[62:67], v[188:191] cbsz:2 blgp:2
	s_waitcnt lgkmcnt(0)
	v_mfma_f32_16x16x128_f8f6f4 v[134:137], v[128:133], v[8:13], v[134:137] cbsz:2 blgp:2
	v_mfma_f32_16x16x128_f8f6f4 v[204:207], v[128:133], v[44:49], v[204:207] cbsz:2 blgp:2
	v_mfma_f32_16x16x128_f8f6f4 v[138:141], v[128:133], v[20:25], v[138:141] cbsz:2 blgp:2
	v_mfma_f32_16x16x128_f8f6f4 v[208:211], v[128:133], v[56:61], v[208:211] cbsz:2 blgp:2
	v_mfma_f32_16x16x128_f8f6f4 v[142:145], v[128:133], v[32:37], v[142:145] cbsz:2 blgp:2
	v_mfma_f32_16x16x128_f8f6f4 v[212:215], v[128:133], v[68:73], v[212:215] cbsz:2 blgp:2
	v_cndmask_b32_e64 v158, v134, v204, s[0:1]
	v_cndmask_b32_e64 v159, v138, v208, s[0:1]
	v_fma_mix_f32 v158, v158, v100, v149 op_sel:[0,0,1] op_sel_hi:[0,0,1]
	v_fma_mix_f32 v159, v159, v101, v153 op_sel:[0,0,1] op_sel_hi:[0,0,1]
	v_exp_f32_e32 v158, v158
	v_exp_f32_e32 v159, v159
	v_fma_f32 v158, v158, v186, v186
	v_add_f32_e32 v159, 1.0, v159
	v_rcp_f32_e32 v158, v158
	v_rcp_f32_e32 v159, v159
	v_cndmask_b32_e64 v160, v142, v212, s[0:1]
	v_fma_mix_f32 v161, v158, v160, v157 op_sel:[0,0,1] op_sel_hi:[0,0,1]
	v_exp_f32_e32 v161, v161
	s_add_u32 s48, s48, s40
	v_add_f32_e32 v161, 1.0, v161
	v_rcp_f32_e32 v161, v161
	s_addc_u32 s49, s49, s41
	v_fma_f32 v162, v161, -2.0, 1.0
	v_sub_f32_e32 v163, v176, v162
	v_fma_f32 v176, v159, v163, v162
	v_fma_f32 v164, |v176|, s17, v113
	v_fma_f32 v165, |v176|, s18, v114
	v_fma_f32 v166, |v176|, s19, v115
	v_lshrrev_b32_e32 v167, 26, v176
	v_min3_u32 v164, v164, v165, v166
	v_bfi_b32 v168, 31, v164, v167
	s_nop 1
	v_mul_u32_u24_dpp v170, v168, v180 quad_perm:[1,2,3,3] row_mask:0xf bank_mask:0xf bound_ctrl:1
	v_mad_u32_u24 v171, v168, v181, v170
	ds_write_b8_d16_hi v184, v171
	s_barrier
	global_store_short_d16_hi v185, v176, s[48:49]
	s_cmp_lt_i32 s44, s45
	s_cbranch_scc1 .Lscan_loop_b_f2
	s_waitcnt lgkmcnt(0)
	s_barrier
